# MoE: waves skip MFMA groups of all-padding 16-row fragments in main K loop (checked loop copy), unit deal rotated per iteration; on top of deferred MFMA group
# speedup vs baseline: 1.0233x; 1.0117x over previous
; #define LAS __attribute__((address_space(3)))
; #define OPAQUE_LDS(p) asm volatile("" : "+v"(p))
; #define G_SETUP(u) do { G_SETUP_B(u); G_SETUP_A(u); } while (0)
;     ...
;     G_SETUP(cur);
;     const int hl = lane >> 5, sc = (lane & 31) * 4;
;     const unsigned vob = (unsigned)((2 * wid + hl) * ldb + sc) * 4u;
;     const unsigned kstepB = (unsigned)ldb * 64u;
;     const int pos0 = (GU ? (sc >> 5) * 64 : (sc & ~31)) + ((sc >> 2) & 1) * 16 + ((sc >> 3) & 3) * 4;
;     LAS unsigned char* b_wr = lds + G_BREG + (((2 * wid + hl) ^ (wid & 4)) * G_BSTRIDE) + pos0 * 2; OPAQUE_LDS(b_wr);
;     constexpr int SLAB1 = GU ? 64 : 256;
;     LAS unsigned char* a_rd = lds + G_AREG + wr * (MF * 2048) + ((fr * 64 + fq * 16) ^ (((fr >> 3) & 1) << 5)); OPAQUE_LDS(a_rd);
;     const int q = (lane & 15) >> 2, p = lane & 3;
;     LAS unsigned char* b_rd0 = lds + G_BREG + fq * (8 * G_BSTRIDE) + (((fq & 1) * 4 + q) * G_BSTRIDE) + wc * 128 + p * 8; OPAQUE_LDS(b_rd0);
;     LAS unsigned char* b_rd1 = lds + G_BREG + fq * (8 * G_BSTRIDE) + ((((fq & 1) ^ 1) * 4 + q) * G_BSTRIDE) + wc * 128 + p * 8; OPAQUE_LDS(b_rd1);
.LBB0_646:
	s_andn2_b64 vcc, exec, s[18:19]
	s_cbranch_vccnz .LBB0_664
	s_lshl_b32 s6, s16, 13
	s_ashr_i32 s7, s6, 31
	s_lshl_b32 s18, s17, 10
	s_lshl_b64 s[6:7], s[6:7], 2
	s_add_u32 s66, s74, s6
	s_addc_u32 s67, s75, s7
	s_ashr_i32 s17, s16, 31
	s_lshl_b64 s[6:7], s[16:17], 24
	s_add_u32 s17, s8, s6
	s_mul_i32 s78, s22, 0x120
	s_addc_u32 s22, s9, s7
	s_mul_i32 s100, s72, 0x90
	s_sub_i32 s99, s65, s78
	s_sub_i32 s99, s99, s100
	s_add_i32 s99, s99, 15
	s_max_i32 s99, s99, 0
	s_lshr_b32 s99, s99, 4
	s_min_u32 s99, s99, 9
	s_lshl_b32 s19, s90, 7
	s_and_b32 s76, s19, 0x380
	s_or_b32 s54, s18, s76
	s_ashr_i32 s55, s54, 31
	s_lshl_b64 s[18:19], s[54:55], 2
	s_add_u32 s55, s17, s18
	s_addc_u32 s77, s22, s19
	s_add_u32 s6, s12, s6
	s_addc_u32 s7, s13, s7
	s_add_u32 s79, s6, s18
	s_addc_u32 s80, s7, s19
	s_lshl_b32 s6, s16, 11
	s_ashr_i32 s7, s6, 31
	s_lshl_b64 s[6:7], s[6:7], 2
	s_add_u32 s56, s10, s6
	s_addc_u32 s57, s11, s7
	s_add_u32 s58, s14, s6
	s_addc_u32 s59, s15, s7
	v_mbcnt_lo_u32_b32 v1, -1, 0
	v_mbcnt_hi_u32_b32 v1, -1, v1
	s_lshl_b32 s6, s89, 3
	v_ashrrev_i32_e32 v2, 2, v1
	v_writelane_b32 v242, s92, 8
	s_and_b32 s81, s6, 0x1ffffff0
	v_add_u32_e32 v2, s78, v2
	s_and_b32 s82, s6, 16
	v_writelane_b32 v242, s93, 9
	s_mov_b32 s24, s90
	v_add_u32_e32 v3, s81, v2
	s_add_i32 s7, s65, -1
	s_bitset1_b32 s82, 8
	v_writelane_b32 v242, s24, 10
	s_mov_b32 s19, 0x20000
	s_mov_b32 s18, 0x7ffffff0
	s_waitcnt vmcnt(18)
	v_min_i32_e32 v4, s7, v3
	v_add_u32_e32 v5, 64, v3
	v_add_u32_e32 v6, 0x80, v3
	v_add_u32_e32 v3, 0xc0, v3
	v_add_u32_e32 v2, s82, v2
	v_writelane_b32 v242, s25, 11
	s_and_b32 s25, s67, 0xffff
	s_mov_b32 s24, s66
	s_mov_b32 s26, s18
	s_mov_b32 s27, s19
	v_lshlrev_b32_e32 v4, 2, v4
	v_min_i32_e32 v5, s7, v5
	v_min_i32_e32 v6, s7, v6
	v_min_i32_e32 v3, s7, v3
	v_min_i32_e32 v2, s7, v2
	buffer_load_dword v4, v4, s[24:27], 0 offen
	v_lshlrev_b32_e32 v5, 2, v5
	v_lshlrev_b32_e32 v6, 2, v6
	v_lshlrev_b32_e32 v3, 2, v3
	v_lshlrev_b32_e32 v2, 2, v2
	buffer_load_dword v5, v5, s[24:27], 0 offen
	s_nop 0
	buffer_load_dword v6, v6, s[24:27], 0 offen
	s_nop 0
	buffer_load_dword v3, v3, s[24:27], 0 offen
	s_nop 0
	buffer_load_dword v2, v2, s[24:27], 0 offen
	v_lshlrev_b32_e32 v13, 4, v1
	v_and_b32_e32 v1, 32, v1
	v_bitop3_b32 v1, v13, v1, 48 bitop3:0x6c
	s_and_b32 s84, s88, 64
	s_movk_i32 s83, 0xf000
	v_or_b32_e32 v1, s84, v1
	s_waitcnt vmcnt(22)
	v_and_b32_e32 v8, 15, v0
	v_lshlrev_b32_e32 v10, 2, v0
	s_mul_i32 s22, s72, 0x4800
	s_add_i32 s22, s22, 0
	v_ashrrev_i32_e32 v7, 4, v0
	v_ashrrev_i32_e32 v9, 5, v0
	v_lshlrev_b32_e32 v11, 4, v0
	v_lshl_add_u32 v9, s89, 1, v9
	v_and_b32_e32 v14, 0x1f0, v11
	s_add_i32 s7, 0, 0x12000
	s_movk_i32 s6, 0x220
	v_lshl_or_b32 v184, v9, 13, v14
	v_bitop3_b32 v9, v9, s89, 4 bitop3:0x78
	v_lshlrev_b32_e32 v12, 5, v0
	v_and_b32_e32 v11, 0x180, v11
	v_mul_lo_u32 v9, v9, s6
	v_and_b32_e32 v12, 32, v12
	v_and_b32_e32 v15, 24, v10
	s_and_b32 s21, s21, 0xffff
	v_add3_u32 v9, s7, v9, v11
	s_mov_b32 s40, s20
	s_mov_b32 s42, s18
	s_mov_b32 s43, s19
	s_and_b32 s25, s77, 0xffff
	s_mov_b32 s41, s21
	v_add3_u32 v185, v9, v12, v15
	s_mov_b32 s16, s55
	s_and_b32 s29, s80, 0xffff
	s_mov_b32 s45, s88
	s_mov_b32 s17, s25
	s_mov_b32 s87, 0x40000
	s_mov_b32 s88, 0x60000
	s_mov_b32 s38, s18
	s_mov_b32 s39, s19
	s_mov_b32 s36, s79
	s_mov_b32 s37, s29
	s_mov_b32 s69, s89
	s_add_i32 s68, s5, s78
	s_mov_b32 s24, s55
	s_mov_b32 s23, s19
	s_mov_b32 s28, s79
	s_mov_b32 s92, 0
	s_waitcnt vmcnt(4)
	v_lshlrev_b32_e32 v4, 10, v4
	v_and_or_b32 v189, v4, s83, v1
	s_waitcnt vmcnt(3)
	v_lshlrev_b32_e32 v4, 10, v5
	s_waitcnt vmcnt(2)
	v_lshlrev_b32_e32 v5, 10, v6
	s_waitcnt vmcnt(1)
	v_lshlrev_b32_e32 v3, 10, v3
	s_waitcnt vmcnt(0)
	v_lshlrev_b32_e32 v2, 10, v2
	v_and_or_b32 v192, v4, s83, v1
	v_and_or_b32 v191, v5, s83, v1
	v_and_or_b32 v190, v3, s83, v1
	v_and_or_b32 v193, v2, s83, v1
	v_and_b32_e32 v1, -16, v0
	v_lshl_add_u32 v1, v8, 6, v1
	v_and_b32_e32 v2, 32, v10
	v_xad_u32 v186, v1, v2, s22
	s_movk_i32 s22, 0x1100
	v_bfe_u32 v1, v0, 2, 2
	v_mul_lo_u32 v2, v7, s22
	v_lshlrev_b32_e32 v3, 2, v7
	v_add_u32_e32 v2, s7, v2
	v_and_or_b32 v4, v3, 4, v1
	v_bitop3_b32 v1, v3, 4, v1 bitop3:0x26
	v_mad_u32_u24 v4, v4, s6, v2
	v_lshlrev_b32_e32 v0, 3, v0
	v_mad_u32_u24 v1, v1, s6, v2
	s_lshl_b32 s6, s89, 10
	s_lshl_b32 s7, s73, 7
	v_and_b32_e32 v0, 24, v0
	s_add_i32 s46, s6, 0
	v_add3_u32 v187, v4, s7, v0
	v_add3_u32 v188, v1, s7, v0
	s_mov_b32 m0, s46
	s_barrier
; #define G_DMA_A(kt, AO) do { G_DMA1(kt, AO, 0); G_DMA1(kt, AO, 1); G_DMA1(kt, AO, 2); G_DMA1(kt, AO, 3); if (MF == 9) G_DMA5(kt, AO); } while (0)
; #define G_ISSUE_B(kt) do { const unsigned _sb = (unsigned)(kt) * 4u * kstepB; \
;         _Pragma("unroll") for (int _i = 0; _i < 8; ++_i) sb[_i] = bload16(_i < 4 ? rsB0 : rsB1, vob, _sb + (_i & 3) * kstepB); } while (0)
; #define G_WRITE_B(BO) do { \
;         _Pragma("unroll") for (int _i = 0; _i < 8; ++_i) *(LAS u32x2*)(b_wr + (BO) + (_i & 3) * (16 * G_BSTRIDE) + (_i >> 2) * SLAB1) = pack4(__builtin_bit_cast(f32x4, sb[_i])); } while (0)
; #define G_ENDTILE(VM) do { asm volatile("s_waitcnt vmcnt(" #VM ")" ::: "memory"); \
;         asm volatile("s_waitcnt lgkmcnt(0)" ::: "memory"); __builtin_amdgcn_s_barrier(); asm volatile("" ::: "memory"); } while (0)
;     ...
;     __builtin_amdgcn_s_barrier();
;     G_DMA_A(0, G_A0); G_ISSUE_B(0); G_WRITE_B(G_B0);
;     __builtin_amdgcn_sched_barrier(0);
;     G_ISSUE_B(1);
;     __builtin_amdgcn_sched_barrier(0);
;     G_ENDTILE(8);
	buffer_load_dwordx4 v189, s[40:43], 0 offen lds
	buffer_load_dwordx4 v[0:3], v184, s[16:19], 0 offen
	buffer_load_dwordx4 v[4:7], v184, s[16:19], s19 offen
	s_add_i32 s86, s46, 0x2000
	buffer_load_dwordx4 v[8:11], v184, s[16:19], s87 offen
	buffer_load_dwordx4 v[12:15], v184, s[16:19], s88 offen
	buffer_load_dwordx4 v[16:19], v184, s[36:39], 0 offen
	s_mov_b32 m0, s86
	s_add_i32 s89, s46, 0x4000
	buffer_load_dwordx4 v[20:23], v184, s[36:39], s19 offen
	buffer_load_dwordx4 v[24:27], v184, s[36:39], s87 offen
	s_lshl_b32 s6, s73, 10
	buffer_load_dwordx4 v192, s[40:43], 0 offen lds
	s_mov_b32 m0, s89
	s_add_i32 s90, s46, 0x6000
	s_add_i32 s48, s6, 0
	buffer_load_dwordx4 v191, s[40:43], 0 offen lds
	s_mov_b32 m0, s90
	buffer_load_dwordx4 v[28:31], v184, s[36:39], s88 offen
	s_add_i32 s91, s48, 0x8000
	buffer_load_dwordx4 v190, s[40:43], 0 offen lds
	s_mov_b32 m0, s91
	s_mov_b32 s22, s18
	buffer_load_dwordx4 v193, s[40:43], 0 offen lds
	s_waitcnt vmcnt(11)
	v_cvt_pk_bf16_f32 v3, v2, v3
	v_cvt_pk_bf16_f32 v2, v0, v1
	s_waitcnt vmcnt(10)
	v_cvt_pk_bf16_f32 v0, v4, v5
	s_waitcnt vmcnt(9)
	v_cvt_pk_bf16_f32 v4, v8, v9
	s_waitcnt vmcnt(7)
	v_cvt_pk_bf16_f32 v9, v18, v19
	v_cvt_pk_bf16_f32 v8, v16, v17
	v_cvt_pk_bf16_f32 v1, v6, v7
	ds_write2_b64 v185, v[2:3], v[8:9] offset1:8
	s_waitcnt vmcnt(6)
	v_cvt_pk_bf16_f32 v3, v22, v23
	v_cvt_pk_bf16_f32 v2, v20, v21
	v_add_u32_e32 v8, 0x2000, v185
	v_cvt_pk_bf16_f32 v5, v10, v11
	ds_write2_b64 v8, v[0:1], v[2:3] offset0:64 offset1:72
	s_waitcnt vmcnt(5)
	v_cvt_pk_bf16_f32 v1, v26, v27
	v_cvt_pk_bf16_f32 v0, v24, v25
	v_add_u32_e32 v2, 0x4000, v185
	v_cvt_pk_bf16_f32 v7, v14, v15
	v_cvt_pk_bf16_f32 v6, v12, v13
	ds_write2_b64 v2, v[4:5], v[0:1] offset0:128 offset1:136
	s_waitcnt vmcnt(2)
	v_cvt_pk_bf16_f32 v1, v30, v31
	v_cvt_pk_bf16_f32 v0, v28, v29
	v_add_u32_e32 v2, 0x6000, v185
	ds_write2_b64 v2, v[6:7], v[0:1] offset0:192 offset1:200
	s_mov_b32 s93, 0x80000
	s_mov_b32 s95, 0xc0000
	s_mov_b32 s94, 0xa0000
	buffer_load_dwordx4 v[12:15], v184, s[16:19], s93 offen
	buffer_load_dwordx4 v[0:3], v184, s[16:19], s94 offen
	s_mov_b32 s96, 0xe0000
	buffer_load_dwordx4 v[28:31], v184, s[16:19], s95 offen
	buffer_load_dwordx4 v[24:27], v184, s[16:19], s96 offen
	buffer_load_dwordx4 v[20:23], v184, s[36:39], s93 offen
	buffer_load_dwordx4 v[4:7], v184, s[36:39], s94 offen
	buffer_load_dwordx4 v[8:11], v184, s[36:39], s95 offen
	buffer_load_dwordx4 v[16:19], v184, s[36:39], s96 offen
	s_waitcnt vmcnt(8)
	s_add_i32 s97, s4, -2
	s_waitcnt lgkmcnt(0)
	s_barrier
	s_cmp_gt_i32 s4, 2
	s_cselect_b64 s[40:41], -1, 0
	s_lshl_b32 s49, s4, 7
	s_add_i32 s85, s46, 0x9000
	s_add_i32 s7, s46, 0xb000
	s_add_i32 s6, s46, 0xd000
	s_add_i32 s47, s46, 0xf000
	s_add_i32 s48, s48, 0x11000
	s_addk_i32 s49, 0xff80
	s_lshl_b32 s4, s73, 5
	s_add_i32 s5, 0, 0x23040
	s_add_i32 s52, 0, 0x2306c
	s_mov_b32 s53, 0xc0e00000
	v_mov_b32_e32 v194, 0x40e00000
	s_mov_b64 s[30:31], s[22:23]
	s_mov_b64 s[26:27], s[22:23]
	s_branch .LBB0_649

;     ...
;         for (int m = 0; m < MF; ++m)
; #pragma unroll
;             for (int n = 0; n < 4; ++n) acc[m][n] = (f32x4){0.f, 0.f, 0.f, 0.f};
;         for (int t = 0; t < nt - 2; t += 2) {
.LBB0_649:
	s_andn2_b64 vcc, exec, s[40:41]
	v_mov_b32_e32 v175, 0
	s_cbranch_vccnz .LBB0_652
	v_mov_b32_e32 v32, 0
	s_mov_b32 s16, 0
	s_mov_b32 s17, 0x1e0000
	s_movk_i32 s36, 0x100
	v_mov_b32_e32 v33, v32
	v_mov_b32_e32 v34, v32
	v_mov_b32_e32 v35, v32
	v_mov_b32_e32 v36, v32
	v_mov_b32_e32 v37, v32
	v_mov_b32_e32 v38, v32
	v_mov_b32_e32 v39, v32
	v_mov_b32_e32 v40, v32
	v_mov_b32_e32 v41, v32
	v_mov_b32_e32 v42, v32
	v_mov_b32_e32 v43, v32
	v_mov_b32_e32 v44, v32
	v_mov_b32_e32 v45, v32
	v_mov_b32_e32 v46, v32
	v_mov_b32_e32 v47, v32
	v_mov_b32_e32 v48, v32
	v_mov_b32_e32 v49, v32
	v_mov_b32_e32 v50, v32
	v_mov_b32_e32 v51, v32
	v_mov_b32_e32 v52, v32
	v_mov_b32_e32 v53, v32
	v_mov_b32_e32 v54, v32
	v_mov_b32_e32 v55, v32
	v_mov_b32_e32 v56, v32
	v_mov_b32_e32 v57, v32
	v_mov_b32_e32 v58, v32
	v_mov_b32_e32 v59, v32
	v_mov_b32_e32 v68, v32
	v_mov_b32_e32 v69, v32
	v_mov_b32_e32 v70, v32
	v_mov_b32_e32 v71, v32
	v_mov_b32_e32 v76, v32
	v_mov_b32_e32 v77, v32
	v_mov_b32_e32 v78, v32
	v_mov_b32_e32 v79, v32
	v_mov_b32_e32 v60, v32
	v_mov_b32_e32 v61, v32
	v_mov_b32_e32 v62, v32
	v_mov_b32_e32 v63, v32
	v_mov_b32_e32 v64, v32
	v_mov_b32_e32 v65, v32
	v_mov_b32_e32 v66, v32
	v_mov_b32_e32 v67, v32
	v_mov_b32_e32 v72, v32
	v_mov_b32_e32 v73, v32
	v_mov_b32_e32 v74, v32
	v_mov_b32_e32 v75, v32
	v_mov_b32_e32 v80, v32
	v_mov_b32_e32 v81, v32
	v_mov_b32_e32 v82, v32
	v_mov_b32_e32 v83, v32
	v_mov_b32_e32 v84, v32
	v_mov_b32_e32 v85, v32
	v_mov_b32_e32 v86, v32
	v_mov_b32_e32 v87, v32
	v_mov_b32_e32 v96, v32
	v_mov_b32_e32 v97, v32
	v_mov_b32_e32 v98, v32
	v_mov_b32_e32 v99, v32
	v_mov_b32_e32 v104, v32
	v_mov_b32_e32 v105, v32
	v_mov_b32_e32 v106, v32
	v_mov_b32_e32 v107, v32
	v_mov_b32_e32 v108, v32
	v_mov_b32_e32 v109, v32
	v_mov_b32_e32 v110, v32
	v_mov_b32_e32 v111, v32
	v_mov_b32_e32 v88, v32
	v_mov_b32_e32 v89, v32
	v_mov_b32_e32 v90, v32
	v_mov_b32_e32 v91, v32
	v_mov_b32_e32 v92, v32
	v_mov_b32_e32 v93, v32
	v_mov_b32_e32 v94, v32
	v_mov_b32_e32 v95, v32
	v_mov_b32_e32 v100, v32
	v_mov_b32_e32 v101, v32
	v_mov_b32_e32 v102, v32
	v_mov_b32_e32 v103, v32
	v_mov_b32_e32 v112, v32
	v_mov_b32_e32 v113, v32
	v_mov_b32_e32 v114, v32
	v_mov_b32_e32 v115, v32
	v_mov_b32_e32 v116, v32
	v_mov_b32_e32 v117, v32
	v_mov_b32_e32 v118, v32
	v_mov_b32_e32 v119, v32
	v_mov_b32_e32 v128, v32
	v_mov_b32_e32 v129, v32
	v_mov_b32_e32 v130, v32
	v_mov_b32_e32 v131, v32
	v_mov_b32_e32 v136, v32
	v_mov_b32_e32 v137, v32
	v_mov_b32_e32 v138, v32
	v_mov_b32_e32 v139, v32
	v_mov_b32_e32 v140, v32
	v_mov_b32_e32 v141, v32
	v_mov_b32_e32 v142, v32
	v_mov_b32_e32 v143, v32
	v_mov_b32_e32 v120, v32
	v_mov_b32_e32 v121, v32
	v_mov_b32_e32 v122, v32
	v_mov_b32_e32 v123, v32
	v_mov_b32_e32 v124, v32
	v_mov_b32_e32 v125, v32
	v_mov_b32_e32 v126, v32
	v_mov_b32_e32 v127, v32
	v_mov_b32_e32 v132, v32
	v_mov_b32_e32 v133, v32
	v_mov_b32_e32 v134, v32
	v_mov_b32_e32 v135, v32
	v_mov_b32_e32 v144, v32
	v_mov_b32_e32 v145, v32
	v_mov_b32_e32 v146, v32
	v_mov_b32_e32 v147, v32
	v_mov_b32_e32 v148, v32
	v_mov_b32_e32 v149, v32
	v_mov_b32_e32 v150, v32
	v_mov_b32_e32 v151, v32
	v_mov_b32_e32 v152, v32
	v_mov_b32_e32 v153, v32
	v_mov_b32_e32 v154, v32
	v_mov_b32_e32 v155, v32
	v_mov_b32_e32 v156, v32
	v_mov_b32_e32 v157, v32
	v_mov_b32_e32 v158, v32
	v_mov_b32_e32 v159, v32
	v_mov_b32_e32 v160, v32
	v_mov_b32_e32 v161, v32
	v_mov_b32_e32 v162, v32
	v_mov_b32_e32 v163, v32
	v_mov_b32_e32 v164, v32
	v_mov_b32_e32 v165, v32
	v_mov_b32_e32 v166, v32
	v_mov_b32_e32 v167, v32
	v_mov_b32_e32 v168, v32
	v_mov_b32_e32 v169, v32
	v_mov_b32_e32 v170, v32
	v_mov_b32_e32 v171, v32
	v_mov_b32_e32 v172, v32
	v_mov_b32_e32 v173, v32
	v_mov_b32_e32 v174, v32
	v_mov_b32_e32 v175, v32
	v_mov_b32_e32 v218, 0
	v_mov_b32_e32 v219, 0
	v_mov_b32_e32 v220, 0
	v_mov_b32_e32 v221, 0
	v_mov_b32_e32 v238, 0
	v_mov_b32_e32 v239, 0
	v_mov_b32_e32 v240, 0
	v_mov_b32_e32 v241, 0
	v_mov_b32_e32 v244, 0
	v_mov_b32_e32 v245, 0
	v_mov_b32_e32 v246, 0
	v_mov_b32_e32 v247, 0
	v_mov_b32_e32 v248, 0
	v_mov_b32_e32 v249, 0
	v_mov_b32_e32 v250, 0
	v_mov_b32_e32 v251, 0
	v_mov_b32_e32 v252, 0
	v_mov_b32_e32 v253, 0
	v_mov_b32_e32 v254, 0
	v_mov_b32_e32 v255, 0
	s_cmp_lt_u32 s99, 9
	s_cbranch_scc1 .Lchk5_loop

.Lchk5_loop:
	s_mov_b32 m0, s85
	s_add_i32 s37, s36, 0xffffff80
	ds_read_b64_tr_b16 v[178:179], v188
	ds_read_b64_tr_b16 v[176:177], v187
	ds_read_b64_tr_b16 v[180:181], v187 offset:32
	ds_read_b64_tr_b16 v[198:199], v187 offset:64
	ds_read_b64_tr_b16 v[202:203], v187 offset:96
	ds_read_b128 v[206:209], v186
	ds_read_b64_tr_b16 v[182:183], v188 offset:32
	ds_read_b64_tr_b16 v[200:201], v188 offset:64
	ds_read_b64_tr_b16 v[204:205], v188 offset:96
	ds_read_b128 v[210:213], v186 offset:2048
	ds_read_b128 v[214:217], v186 offset:4096
	buffer_load_dwordx4 v189, s[20:23], s37 offen lds
	s_mov_b32 m0, s7
	s_cmp_le_u32 s99, 8
	s_cbranch_scc1 .Lchk5_s1
	v_mfma_f32_16x16x32_bf16 v[44:47], v[244:247], v[238:241], v[44:47]
	v_mfma_f32_16x16x32_bf16 v[40:43], v[218:221], v[238:241], v[40:43]
	v_mfma_f32_16x16x32_bf16 v[36:39], v[248:251], v[238:241], v[36:39]
	v_mfma_f32_16x16x32_bf16 v[32:35], v[252:255], v[238:241], v[32:35]
.Lchk5_s1:
	s_waitcnt lgkmcnt(5)
	s_waitcnt lgkmcnt(4)
	s_waitcnt lgkmcnt(3)
	s_waitcnt lgkmcnt(2)
	s_cmp_le_u32 s99, 0
	s_cbranch_scc1 .Lchk5_s2
	v_mfma_f32_16x16x32_bf16 v[172:175], v[176:179], v[206:209], v[172:175]
	v_mfma_f32_16x16x32_bf16 v[168:171], v[180:183], v[206:209], v[168:171]
	v_mfma_f32_16x16x32_bf16 v[164:167], v[198:201], v[206:209], v[164:167]
	v_mfma_f32_16x16x32_bf16 v[160:163], v[202:205], v[206:209], v[160:163]
.Lchk5_s2:
	buffer_load_dwordx4 v192, s[20:23], s37 offen lds
	s_mov_b32 m0, s6
	s_nop 0
	buffer_load_dwordx4 v191, s[20:23], s37 offen lds
	s_mov_b32 m0, s47
	s_nop 0
	buffer_load_dwordx4 v190, s[20:23], s37 offen lds
	s_mov_b32 m0, s48
	s_nop 0
	buffer_load_dwordx4 v193, s[20:23], s37 offen lds
	s_add_i32 s37, s17, 0xfff20000
	s_waitcnt lgkmcnt(1)
	s_waitcnt vmcnt(12)
	s_cmp_le_u32 s99, 1
	s_cbranch_scc1 .Lchk5_s3
	v_mfma_f32_16x16x32_bf16 v[156:159], v[176:179], v[210:213], v[156:159]
	v_mfma_f32_16x16x32_bf16 v[152:155], v[180:183], v[210:213], v[152:155]
	v_mfma_f32_16x16x32_bf16 v[148:151], v[198:201], v[210:213], v[148:151]
	v_mfma_f32_16x16x32_bf16 v[144:147], v[202:205], v[210:213], v[144:147]
.Lchk5_s3:
	ds_read_b128 v[206:209], v186 offset:6144
	v_cvt_pk_bf16_f32 v15, v14, v15
	v_cvt_pk_bf16_f32 v14, v12, v13
	ds_write_b64 v185, v[14:15] offset:34816
	buffer_load_dwordx4 v[12:15], v184, s[24:27], s37 offen
	s_waitcnt lgkmcnt(2)
	s_cmp_le_u32 s99, 2
	s_cbranch_scc1 .Lchk5_s4
	v_mfma_f32_16x16x32_bf16 v[132:135], v[176:179], v[214:217], v[132:135]
	v_mfma_f32_16x16x32_bf16 v[124:127], v[180:183], v[214:217], v[124:127]
	v_mfma_f32_16x16x32_bf16 v[120:123], v[198:201], v[214:217], v[120:123]
	v_mfma_f32_16x16x32_bf16 v[140:143], v[202:205], v[214:217], v[140:143]
.Lchk5_s4:
	ds_read_b128 v[210:213], v186 offset:8192
	s_waitcnt lgkmcnt(2)
	s_waitcnt vmcnt(12)
	s_cmp_le_u32 s99, 3
	s_cbranch_scc1 .Lchk5_s5
	v_mfma_f32_16x16x32_bf16 v[136:139], v[176:179], v[206:209], v[136:139]
	v_mfma_f32_16x16x32_bf16 v[128:131], v[180:183], v[206:209], v[128:131]
	v_mfma_f32_16x16x32_bf16 v[116:119], v[198:201], v[206:209], v[116:119]
	v_mfma_f32_16x16x32_bf16 v[112:115], v[202:205], v[206:209], v[112:115]
.Lchk5_s5:
	ds_read_b128 v[214:217], v186 offset:10240
	v_cvt_pk_bf16_f32 v3, v2, v3
	v_cvt_pk_bf16_f32 v2, v0, v1
	ds_write_b64 v185, v[2:3] offset:43520
	s_add_i32 s38, s17, 0xfff40000
	buffer_load_dwordx4 v[0:3], v184, s[24:27], s38 offen
	s_waitcnt lgkmcnt(2)
	s_cmp_le_u32 s99, 4
	s_cbranch_scc1 .Lchk5_s6
	v_mfma_f32_16x16x32_bf16 v[100:103], v[176:179], v[210:213], v[100:103]
	v_mfma_f32_16x16x32_bf16 v[92:95], v[180:183], v[210:213], v[92:95]
	v_mfma_f32_16x16x32_bf16 v[88:91], v[198:201], v[210:213], v[88:91]
	v_mfma_f32_16x16x32_bf16 v[108:111], v[202:205], v[210:213], v[108:111]
.Lchk5_s6:
	ds_read_b128 v[206:209], v186 offset:12288
	s_waitcnt lgkmcnt(2)
	s_waitcnt vmcnt(12)
	s_cmp_le_u32 s99, 5
	s_cbranch_scc1 .Lchk5_s7
	v_mfma_f32_16x16x32_bf16 v[104:107], v[176:179], v[214:217], v[104:107]
	v_mfma_f32_16x16x32_bf16 v[96:99], v[180:183], v[214:217], v[96:99]
	v_mfma_f32_16x16x32_bf16 v[84:87], v[198:201], v[214:217], v[84:87]
	v_mfma_f32_16x16x32_bf16 v[80:83], v[202:205], v[214:217], v[80:83]
.Lchk5_s7:
	ds_read_b128 v[210:213], v186 offset:14336
	v_cvt_pk_bf16_f32 v31, v30, v31
	v_cvt_pk_bf16_f32 v30, v28, v29
	ds_write_b64 v185, v[30:31] offset:52224
	s_add_i32 s39, s17, 0xfff60000
	buffer_load_dwordx4 v[28:31], v184, s[24:27], s39 offen
	s_waitcnt lgkmcnt(2)
	s_cmp_le_u32 s99, 6
	s_cbranch_scc1 .Lchk5_s8
	v_mfma_f32_16x16x32_bf16 v[72:75], v[176:179], v[206:209], v[72:75]
	v_mfma_f32_16x16x32_bf16 v[64:67], v[180:183], v[206:209], v[64:67]
	v_mfma_f32_16x16x32_bf16 v[60:63], v[198:201], v[206:209], v[60:63]
	v_mfma_f32_16x16x32_bf16 v[76:79], v[202:205], v[206:209], v[76:79]
.Lchk5_s8:
	ds_read_b128 v[214:217], v186 offset:16384
	s_waitcnt lgkmcnt(2)
	s_waitcnt vmcnt(12)
	s_cmp_le_u32 s99, 7
	s_cbranch_scc1 .Lchk5_s9
	v_mfma_f32_16x16x32_bf16 v[68:71], v[176:179], v[210:213], v[68:71]
	v_mfma_f32_16x16x32_bf16 v[56:59], v[180:183], v[210:213], v[56:59]
	v_mfma_f32_16x16x32_bf16 v[52:55], v[198:201], v[210:213], v[52:55]
	v_mfma_f32_16x16x32_bf16 v[48:51], v[202:205], v[210:213], v[48:51]
.Lchk5_s9:
	ds_read_b128 v[206:209], v186 offset:1024
	v_cvt_pk_bf16_f32 v27, v26, v27
	v_cvt_pk_bf16_f32 v26, v24, v25
	ds_write_b64 v185, v[26:27] offset:60928
	s_add_i32 s42, s17, 0xfff80000
	buffer_load_dwordx4 v[24:27], v184, s[24:27], s42 offen
	ds_read_b128 v[210:213], v186 offset:3072
	s_waitcnt lgkmcnt(3)
	s_cmp_le_u32 s99, 8
	s_cbranch_scc1 .Lchk5_s10
	v_mfma_f32_16x16x32_bf16 v[44:47], v[176:179], v[214:217], v[44:47]
	v_mfma_f32_16x16x32_bf16 v[40:43], v[180:183], v[214:217], v[40:43]
	v_mfma_f32_16x16x32_bf16 v[36:39], v[198:201], v[214:217], v[36:39]
	v_mfma_f32_16x16x32_bf16 v[32:35], v[202:205], v[214:217], v[32:35]
.Lchk5_s10:
	ds_read_b64_tr_b16 v[246:247], v188 offset:17408
	ds_read_b64_tr_b16 v[220:221], v188 offset:17440
	ds_read_b64_tr_b16 v[244:245], v187 offset:17408
	ds_read_b64_tr_b16 v[218:219], v187 offset:17440
	ds_read_b64_tr_b16 v[248:249], v187 offset:17472
	ds_read_b64_tr_b16 v[250:251], v188 offset:17472
	ds_read_b64_tr_b16 v[252:253], v187 offset:17504
	ds_read_b64_tr_b16 v[254:255], v188 offset:17504
	s_waitcnt lgkmcnt(5)
	s_waitcnt vmcnt(12)
	s_waitcnt lgkmcnt(4)
	s_waitcnt lgkmcnt(2)
	s_waitcnt lgkmcnt(0)
	s_cmp_le_u32 s99, 0
	s_cbranch_scc1 .Lchk5_s11
	v_mfma_f32_16x16x32_bf16 v[172:175], v[244:247], v[206:209], v[172:175]
	v_mfma_f32_16x16x32_bf16 v[168:171], v[218:221], v[206:209], v[168:171]
	v_mfma_f32_16x16x32_bf16 v[164:167], v[248:251], v[206:209], v[164:167]
	v_mfma_f32_16x16x32_bf16 v[160:163], v[252:255], v[206:209], v[160:163]
.Lchk5_s11:
	ds_read_b128 v[202:205], v186 offset:5120
	v_cvt_pk_bf16_f32 v23, v22, v23
	v_cvt_pk_bf16_f32 v22, v20, v21
	ds_write_b64 v185, v[22:23] offset:34880
	buffer_load_dwordx4 v[20:23], v184, s[28:31], s37 offen
	s_cmp_le_u32 s99, 1
	s_cbranch_scc1 .Lchk5_s12
	v_mfma_f32_16x16x32_bf16 v[156:159], v[244:247], v[210:213], v[156:159]
	v_mfma_f32_16x16x32_bf16 v[152:155], v[218:221], v[210:213], v[152:155]
	v_mfma_f32_16x16x32_bf16 v[148:151], v[248:251], v[210:213], v[148:151]
	v_mfma_f32_16x16x32_bf16 v[144:147], v[252:255], v[210:213], v[144:147]
.Lchk5_s12:
	ds_read_b128 v[206:209], v186 offset:7168
	s_waitcnt lgkmcnt(2)
	s_waitcnt vmcnt(12)
	s_cmp_le_u32 s99, 2
	s_cbranch_scc1 .Lchk5_s13
	v_mfma_f32_16x16x32_bf16 v[132:135], v[244:247], v[202:205], v[132:135]
	v_mfma_f32_16x16x32_bf16 v[124:127], v[218:221], v[202:205], v[124:127]
	v_mfma_f32_16x16x32_bf16 v[120:123], v[248:251], v[202:205], v[120:123]
	v_mfma_f32_16x16x32_bf16 v[140:143], v[252:255], v[202:205], v[140:143]
.Lchk5_s13:
	ds_read_b128 v[210:213], v186 offset:9216
	v_cvt_pk_bf16_f32 v7, v6, v7
	v_cvt_pk_bf16_f32 v6, v4, v5
	ds_write_b64 v185, v[6:7] offset:43584
	buffer_load_dwordx4 v[4:7], v184, s[28:31], s38 offen
	s_waitcnt lgkmcnt(2)
	s_cmp_le_u32 s99, 3
	s_cbranch_scc1 .Lchk5_s14
	v_mfma_f32_16x16x32_bf16 v[136:139], v[244:247], v[206:209], v[136:139]
	v_mfma_f32_16x16x32_bf16 v[128:131], v[218:221], v[206:209], v[128:131]
	v_mfma_f32_16x16x32_bf16 v[116:119], v[248:251], v[206:209], v[116:119]
	v_mfma_f32_16x16x32_bf16 v[112:115], v[252:255], v[206:209], v[112:115]
.Lchk5_s14:
	ds_read_b128 v[202:205], v186 offset:11264
	s_waitcnt lgkmcnt(2)
	s_waitcnt vmcnt(12)
	s_cmp_le_u32 s99, 4
	s_cbranch_scc1 .Lchk5_s15
	v_mfma_f32_16x16x32_bf16 v[100:103], v[244:247], v[210:213], v[100:103]
	v_mfma_f32_16x16x32_bf16 v[92:95], v[218:221], v[210:213], v[92:95]
	v_mfma_f32_16x16x32_bf16 v[88:91], v[248:251], v[210:213], v[88:91]
	v_mfma_f32_16x16x32_bf16 v[108:111], v[252:255], v[210:213], v[108:111]
.Lchk5_s15:
	ds_read_b128 v[206:209], v186 offset:13312
	v_cvt_pk_bf16_f32 v11, v10, v11
	v_cvt_pk_bf16_f32 v10, v8, v9
	ds_write_b64 v185, v[10:11] offset:52288
	buffer_load_dwordx4 v[8:11], v184, s[28:31], s39 offen
	s_waitcnt lgkmcnt(2)
	s_cmp_le_u32 s99, 5
	s_cbranch_scc1 .Lchk5_s16
	v_mfma_f32_16x16x32_bf16 v[104:107], v[244:247], v[202:205], v[104:107]
	v_mfma_f32_16x16x32_bf16 v[96:99], v[218:221], v[202:205], v[96:99]
	v_mfma_f32_16x16x32_bf16 v[84:87], v[248:251], v[202:205], v[84:87]
	v_mfma_f32_16x16x32_bf16 v[80:83], v[252:255], v[202:205], v[80:83]
.Lchk5_s16:
	ds_read_b128 v[210:213], v186 offset:15360
	s_waitcnt lgkmcnt(2)
	s_waitcnt vmcnt(12)
	s_cmp_le_u32 s99, 6
	s_cbranch_scc1 .Lchk5_s17
	v_mfma_f32_16x16x32_bf16 v[72:75], v[244:247], v[206:209], v[72:75]
	v_mfma_f32_16x16x32_bf16 v[64:67], v[218:221], v[206:209], v[64:67]
	v_mfma_f32_16x16x32_bf16 v[60:63], v[248:251], v[206:209], v[60:63]
	v_mfma_f32_16x16x32_bf16 v[76:79], v[252:255], v[206:209], v[76:79]
.Lchk5_s17:
	ds_read_b128 v[238:241], v186 offset:17408
	v_cvt_pk_bf16_f32 v19, v18, v19
	v_cvt_pk_bf16_f32 v18, v16, v17
	ds_write_b64 v185, v[18:19] offset:60992
	buffer_load_dwordx4 v[16:19], v184, s[28:31], s42 offen
	s_waitcnt lgkmcnt(2)
	s_cmp_le_u32 s99, 7
	s_cbranch_scc1 .Lchk5_s18
	v_mfma_f32_16x16x32_bf16 v[68:71], v[244:247], v[210:213], v[68:71]
	v_mfma_f32_16x16x32_bf16 v[56:59], v[218:221], v[210:213], v[56:59]
	v_mfma_f32_16x16x32_bf16 v[52:55], v[248:251], v[210:213], v[52:55]
	v_mfma_f32_16x16x32_bf16 v[48:51], v[252:255], v[210:213], v[48:51]
.Lchk5_s18:
	s_waitcnt lgkmcnt(1)
	s_waitcnt vmcnt(8)
	s_mov_b32 m0, s46
	s_waitcnt lgkmcnt(0)
	s_barrier
	ds_read_b64_tr_b16 v[178:179], v188 offset:34816
	ds_read_b64_tr_b16 v[176:177], v187 offset:34816
	ds_read_b64_tr_b16 v[180:181], v187 offset:34848
	ds_read_b64_tr_b16 v[198:199], v187 offset:34880
	ds_read_b64_tr_b16 v[202:203], v187 offset:34912
	ds_read_b128 v[206:209], v186 offset:36864
	ds_read_b64_tr_b16 v[182:183], v188 offset:34848
	ds_read_b64_tr_b16 v[200:201], v188 offset:34880
	ds_read_b64_tr_b16 v[204:205], v188 offset:34912
	ds_read_b128 v[210:213], v186 offset:38912
	ds_read_b128 v[214:217], v186 offset:40960
	buffer_load_dwordx4 v189, s[20:23], s36 offen lds
	s_mov_b32 m0, s86
	s_cmp_le_u32 s99, 8
	s_cbranch_scc1 .Lchk5_s19
	v_mfma_f32_16x16x32_bf16 v[44:47], v[244:247], v[238:241], v[44:47]
	v_mfma_f32_16x16x32_bf16 v[40:43], v[218:221], v[238:241], v[40:43]
	v_mfma_f32_16x16x32_bf16 v[36:39], v[248:251], v[238:241], v[36:39]
	v_mfma_f32_16x16x32_bf16 v[32:35], v[252:255], v[238:241], v[32:35]

.Lchk5_s20:
	buffer_load_dwordx4 v192, s[20:23], s36 offen lds
	s_mov_b32 m0, s89
	s_add_i32 s37, s17, 0xfffa0000
	buffer_load_dwordx4 v191, s[20:23], s36 offen lds
	s_mov_b32 m0, s90
	s_nop 0
	buffer_load_dwordx4 v190, s[20:23], s36 offen lds
	s_mov_b32 m0, s91
	s_nop 0
	buffer_load_dwordx4 v193, s[20:23], s36 offen lds
	s_waitcnt lgkmcnt(1)
	s_waitcnt vmcnt(12)
	s_cmp_le_u32 s99, 1
	s_cbranch_scc1 .Lchk5_s21
	v_mfma_f32_16x16x32_bf16 v[156:159], v[176:179], v[210:213], v[156:159]
	v_mfma_f32_16x16x32_bf16 v[152:155], v[180:183], v[210:213], v[152:155]
	v_mfma_f32_16x16x32_bf16 v[148:151], v[198:201], v[210:213], v[148:151]
	v_mfma_f32_16x16x32_bf16 v[144:147], v[202:205], v[210:213], v[144:147]
.Lchk5_s21:
	ds_read_b128 v[206:209], v186 offset:43008
	v_cvt_pk_bf16_f32 v15, v14, v15
	v_cvt_pk_bf16_f32 v14, v12, v13
	ds_write_b64 v185, v[14:15]
	buffer_load_dwordx4 v[12:15], v184, s[24:27], s37 offen
	s_waitcnt lgkmcnt(2)
	s_cmp_le_u32 s99, 2
	s_cbranch_scc1 .Lchk5_s22
	v_mfma_f32_16x16x32_bf16 v[132:135], v[176:179], v[214:217], v[132:135]
	v_mfma_f32_16x16x32_bf16 v[124:127], v[180:183], v[214:217], v[124:127]
	v_mfma_f32_16x16x32_bf16 v[120:123], v[198:201], v[214:217], v[120:123]
	v_mfma_f32_16x16x32_bf16 v[140:143], v[202:205], v[214:217], v[140:143]
.Lchk5_s22:
	ds_read_b128 v[210:213], v186 offset:45056
	s_waitcnt lgkmcnt(2)
	s_waitcnt vmcnt(12)
	s_cmp_le_u32 s99, 3
	s_cbranch_scc1 .Lchk5_s23
	v_mfma_f32_16x16x32_bf16 v[136:139], v[176:179], v[206:209], v[136:139]
	v_mfma_f32_16x16x32_bf16 v[128:131], v[180:183], v[206:209], v[128:131]
	v_mfma_f32_16x16x32_bf16 v[116:119], v[198:201], v[206:209], v[116:119]
	v_mfma_f32_16x16x32_bf16 v[112:115], v[202:205], v[206:209], v[112:115]
.Lchk5_s23:
	ds_read_b128 v[214:217], v186 offset:47104
	v_cvt_pk_bf16_f32 v3, v2, v3
	v_cvt_pk_bf16_f32 v2, v0, v1
	ds_write_b64 v185, v[2:3] offset:8704
	s_add_i32 s38, s17, 0xfffc0000
	buffer_load_dwordx4 v[0:3], v184, s[24:27], s38 offen
	s_waitcnt lgkmcnt(2)
	s_cmp_le_u32 s99, 4
	s_cbranch_scc1 .Lchk5_s24
	v_mfma_f32_16x16x32_bf16 v[100:103], v[176:179], v[210:213], v[100:103]
	v_mfma_f32_16x16x32_bf16 v[92:95], v[180:183], v[210:213], v[92:95]
	v_mfma_f32_16x16x32_bf16 v[88:91], v[198:201], v[210:213], v[88:91]
	v_mfma_f32_16x16x32_bf16 v[108:111], v[202:205], v[210:213], v[108:111]
.Lchk5_s24:
	ds_read_b128 v[206:209], v186 offset:49152
	s_waitcnt lgkmcnt(2)
	s_waitcnt vmcnt(12)
	s_cmp_le_u32 s99, 5
	s_cbranch_scc1 .Lchk5_s25
	v_mfma_f32_16x16x32_bf16 v[104:107], v[176:179], v[214:217], v[104:107]
	v_mfma_f32_16x16x32_bf16 v[96:99], v[180:183], v[214:217], v[96:99]
	v_mfma_f32_16x16x32_bf16 v[84:87], v[198:201], v[214:217], v[84:87]
	v_mfma_f32_16x16x32_bf16 v[80:83], v[202:205], v[214:217], v[80:83]
.Lchk5_s25:
	ds_read_b128 v[210:213], v186 offset:51200
	v_cvt_pk_bf16_f32 v31, v30, v31
	v_cvt_pk_bf16_f32 v30, v28, v29
	ds_write_b64 v185, v[30:31] offset:17408
	s_add_i32 s39, s17, 0xfffe0000
	buffer_load_dwordx4 v[28:31], v184, s[24:27], s39 offen
	s_waitcnt lgkmcnt(2)
	s_cmp_le_u32 s99, 6
	s_cbranch_scc1 .Lchk5_s26
	v_mfma_f32_16x16x32_bf16 v[72:75], v[176:179], v[206:209], v[72:75]
	v_mfma_f32_16x16x32_bf16 v[64:67], v[180:183], v[206:209], v[64:67]
	v_mfma_f32_16x16x32_bf16 v[60:63], v[198:201], v[206:209], v[60:63]
	v_mfma_f32_16x16x32_bf16 v[76:79], v[202:205], v[206:209], v[76:79]
.Lchk5_s26:
	ds_read_b128 v[214:217], v186 offset:53248
	s_waitcnt lgkmcnt(2)
	s_waitcnt vmcnt(12)
	s_cmp_le_u32 s99, 7
	s_cbranch_scc1 .Lchk5_s27
	v_mfma_f32_16x16x32_bf16 v[68:71], v[176:179], v[210:213], v[68:71]
	v_mfma_f32_16x16x32_bf16 v[56:59], v[180:183], v[210:213], v[56:59]
	v_mfma_f32_16x16x32_bf16 v[52:55], v[198:201], v[210:213], v[52:55]
	v_mfma_f32_16x16x32_bf16 v[48:51], v[202:205], v[210:213], v[48:51]
.Lchk5_s27:
	ds_read_b128 v[206:209], v186 offset:37888
	v_cvt_pk_bf16_f32 v27, v26, v27
	v_cvt_pk_bf16_f32 v26, v24, v25
	ds_write_b64 v185, v[26:27] offset:26112
	buffer_load_dwordx4 v[24:27], v184, s[24:27], s17 offen
	ds_read_b128 v[210:213], v186 offset:39936
	s_waitcnt lgkmcnt(3)
	s_cmp_le_u32 s99, 8
	s_cbranch_scc1 .Lchk5_s28
	v_mfma_f32_16x16x32_bf16 v[44:47], v[176:179], v[214:217], v[44:47]
	v_mfma_f32_16x16x32_bf16 v[40:43], v[180:183], v[214:217], v[40:43]
	v_mfma_f32_16x16x32_bf16 v[36:39], v[198:201], v[214:217], v[36:39]
	v_mfma_f32_16x16x32_bf16 v[32:35], v[202:205], v[214:217], v[32:35]
; #define G_DMA_A(kt, AO) do { G_DMA1(kt, AO, 0); G_DMA1(kt, AO, 1); G_DMA1(kt, AO, 2); G_DMA1(kt, AO, 3); if (MF == 9) G_DMA5(kt, AO); } while (0)
; #define G_ISSUE_B(kt) do { const unsigned _sb = (unsigned)(kt) * 4u * kstepB; \
;         _Pragma("unroll") for (int _i = 0; _i < 8; ++_i) sb[_i] = bload16(_i < 4 ? rsB0 : rsB1, vob, _sb + (_i & 3) * kstepB); } while (0)
; #define G_WRITE_B(BO) do { \
;         _Pragma("unroll") for (int _i = 0; _i < 8; ++_i) *(LAS u32x2*)(b_wr + (BO) + (_i & 3) * (16 * G_BSTRIDE) + (_i >> 2) * SLAB1) = pack4(__builtin_bit_cast(f32x4, sb[_i])); } while (0)
; #define G_ENDTILE(VM) do { asm volatile("s_waitcnt vmcnt(" #VM ")" ::: "memory"); \
;         asm volatile("s_waitcnt lgkmcnt(0)" ::: "memory"); __builtin_amdgcn_s_barrier(); asm volatile("" ::: "memory"); } while (0)
;     ...
;     __builtin_amdgcn_s_barrier();
;     G_DMA_A(0, G_A0); G_ISSUE_B(0); G_WRITE_B(G_B0);
;     __builtin_amdgcn_sched_barrier(0);
;     G_ISSUE_B(1);
;     __builtin_amdgcn_sched_barrier(0);
;     G_ENDTILE(8);
;     for (int ui = 0;; ++ui) {
; #pragma unroll
;         for (int m = 0; m < MF; ++m)
; #pragma unroll
;             for (int n = 0; n < 4; ++n) acc[m][n] = (f32x4){0.f, 0.f, 0.f, 0.f};
;         for (int t = 0; t < nt - 2; t += 2) {
;             G_TILE(G_A0, G_B0, true, G_B1, G_A1, t + 1, true, t + 2, (void)0);
;             G_ENDTILE(8);
;             G_TILE(G_A1, G_B1, true, G_B0, G_A0, t + 2, true, t + 3, (void)0);
;             G_ENDTILE(8);
;         }
.Lchk5_s28:
	ds_read_b64_tr_b16 v[246:247], v188 offset:52224
	ds_read_b64_tr_b16 v[220:221], v188 offset:52256
	ds_read_b64_tr_b16 v[244:245], v187 offset:52224
	ds_read_b64_tr_b16 v[218:219], v187 offset:52256
	ds_read_b64_tr_b16 v[248:249], v187 offset:52288
	ds_read_b64_tr_b16 v[250:251], v188 offset:52288
	ds_read_b64_tr_b16 v[252:253], v187 offset:52320
	ds_read_b64_tr_b16 v[254:255], v188 offset:52320
	s_waitcnt lgkmcnt(5)
	s_waitcnt vmcnt(12)
	s_waitcnt lgkmcnt(4)
	s_waitcnt lgkmcnt(2)
	s_waitcnt lgkmcnt(0)
	s_cmp_le_u32 s99, 0
	s_cbranch_scc1 .Lchk5_s29
	v_mfma_f32_16x16x32_bf16 v[172:175], v[244:247], v[206:209], v[172:175]
	v_mfma_f32_16x16x32_bf16 v[168:171], v[218:221], v[206:209], v[168:171]
	v_mfma_f32_16x16x32_bf16 v[164:167], v[248:251], v[206:209], v[164:167]
	v_mfma_f32_16x16x32_bf16 v[160:163], v[252:255], v[206:209], v[160:163]
.Lchk5_s29:
	ds_read_b128 v[202:205], v186 offset:41984
	v_cvt_pk_bf16_f32 v23, v22, v23
	v_cvt_pk_bf16_f32 v22, v20, v21
	ds_write_b64 v185, v[22:23] offset:64
	buffer_load_dwordx4 v[20:23], v184, s[28:31], s37 offen
	s_cmp_le_u32 s99, 1
	s_cbranch_scc1 .Lchk5_s30
	v_mfma_f32_16x16x32_bf16 v[156:159], v[244:247], v[210:213], v[156:159]
	v_mfma_f32_16x16x32_bf16 v[152:155], v[218:221], v[210:213], v[152:155]
	v_mfma_f32_16x16x32_bf16 v[148:151], v[248:251], v[210:213], v[148:151]
	v_mfma_f32_16x16x32_bf16 v[144:147], v[252:255], v[210:213], v[144:147]
.Lchk5_s30:
	ds_read_b128 v[206:209], v186 offset:44032
	s_waitcnt lgkmcnt(2)
	s_waitcnt vmcnt(12)
	s_cmp_le_u32 s99, 2
	s_cbranch_scc1 .Lchk5_s31
	v_mfma_f32_16x16x32_bf16 v[132:135], v[244:247], v[202:205], v[132:135]
	v_mfma_f32_16x16x32_bf16 v[124:127], v[218:221], v[202:205], v[124:127]
	v_mfma_f32_16x16x32_bf16 v[120:123], v[248:251], v[202:205], v[120:123]
	v_mfma_f32_16x16x32_bf16 v[140:143], v[252:255], v[202:205], v[140:143]
.Lchk5_s31:
	ds_read_b128 v[210:213], v186 offset:46080
	v_cvt_pk_bf16_f32 v7, v6, v7
	v_cvt_pk_bf16_f32 v6, v4, v5
	ds_write_b64 v185, v[6:7] offset:8768
	buffer_load_dwordx4 v[4:7], v184, s[28:31], s38 offen
	s_waitcnt lgkmcnt(2)
	s_cmp_le_u32 s99, 3
	s_cbranch_scc1 .Lchk5_s32
	v_mfma_f32_16x16x32_bf16 v[136:139], v[244:247], v[206:209], v[136:139]
	v_mfma_f32_16x16x32_bf16 v[128:131], v[218:221], v[206:209], v[128:131]
	v_mfma_f32_16x16x32_bf16 v[116:119], v[248:251], v[206:209], v[116:119]
	v_mfma_f32_16x16x32_bf16 v[112:115], v[252:255], v[206:209], v[112:115]
.Lchk5_s32:
	ds_read_b128 v[202:205], v186 offset:48128
	s_waitcnt lgkmcnt(2)
	s_waitcnt vmcnt(12)
	s_cmp_le_u32 s99, 4
	s_cbranch_scc1 .Lchk5_s33
	v_mfma_f32_16x16x32_bf16 v[100:103], v[244:247], v[210:213], v[100:103]
	v_mfma_f32_16x16x32_bf16 v[92:95], v[218:221], v[210:213], v[92:95]
	v_mfma_f32_16x16x32_bf16 v[88:91], v[248:251], v[210:213], v[88:91]
	v_mfma_f32_16x16x32_bf16 v[108:111], v[252:255], v[210:213], v[108:111]
.Lchk5_s33:
	ds_read_b128 v[206:209], v186 offset:50176
	v_cvt_pk_bf16_f32 v11, v10, v11
	v_cvt_pk_bf16_f32 v10, v8, v9
	ds_write_b64 v185, v[10:11] offset:17472
	buffer_load_dwordx4 v[8:11], v184, s[28:31], s39 offen
	s_waitcnt lgkmcnt(2)
	s_cmp_le_u32 s99, 5
	s_cbranch_scc1 .Lchk5_s34
	v_mfma_f32_16x16x32_bf16 v[104:107], v[244:247], v[202:205], v[104:107]
	v_mfma_f32_16x16x32_bf16 v[96:99], v[218:221], v[202:205], v[96:99]
	v_mfma_f32_16x16x32_bf16 v[84:87], v[248:251], v[202:205], v[84:87]
	v_mfma_f32_16x16x32_bf16 v[80:83], v[252:255], v[202:205], v[80:83]
.Lchk5_s34:
	ds_read_b128 v[210:213], v186 offset:52224
	s_waitcnt lgkmcnt(2)
	s_waitcnt vmcnt(12)
	s_cmp_le_u32 s99, 6
	s_cbranch_scc1 .Lchk5_s35
	v_mfma_f32_16x16x32_bf16 v[72:75], v[244:247], v[206:209], v[72:75]
	v_mfma_f32_16x16x32_bf16 v[64:67], v[218:221], v[206:209], v[64:67]
	v_mfma_f32_16x16x32_bf16 v[60:63], v[248:251], v[206:209], v[60:63]
	v_mfma_f32_16x16x32_bf16 v[76:79], v[252:255], v[206:209], v[76:79]
.Lchk5_s35:
	ds_read_b128 v[238:241], v186 offset:54272
	v_cvt_pk_bf16_f32 v19, v18, v19
	v_cvt_pk_bf16_f32 v18, v16, v17
	ds_write_b64 v185, v[18:19] offset:26176
	buffer_load_dwordx4 v[16:19], v184, s[28:31], s17 offen
	s_waitcnt lgkmcnt(2)
	s_cmp_le_u32 s99, 7
	s_cbranch_scc1 .Lchk5_s36
	v_mfma_f32_16x16x32_bf16 v[68:71], v[244:247], v[210:213], v[68:71]
	v_mfma_f32_16x16x32_bf16 v[56:59], v[218:221], v[210:213], v[56:59]
	v_mfma_f32_16x16x32_bf16 v[52:55], v[248:251], v[210:213], v[52:55]
	v_mfma_f32_16x16x32_bf16 v[48:51], v[252:255], v[210:213], v[48:51]
.Lchk5_s36:
	s_waitcnt lgkmcnt(1)
	s_waitcnt vmcnt(8)
	s_waitcnt lgkmcnt(0)
	s_barrier
	s_add_i32 s16, s16, 2
	s_add_i32 s17, s17, 0x100000
	s_addk_i32 s36, 0x100
	s_cmp_ge_i32 s16, s97
	s_cbranch_scc0 .Lchk5_loop
	s_cmp_le_u32 s99, 8
	s_cbranch_scc1 .Lchk5_s37
	v_mfma_f32_16x16x32_bf16 v[44:47], v[244:247], v[238:241], v[44:47]
	v_mfma_f32_16x16x32_bf16 v[40:43], v[218:221], v[238:241], v[40:43]
	v_mfma_f32_16x16x32_bf16 v[36:39], v[248:251], v[238:241], v[36:39]
	v_mfma_f32_16x16x32_bf16 v[32:35], v[252:255], v[238:241], v[32:35]
.Lchk5_s37:
	s_branch .LBB0_653

; #define LAS __attribute__((address_space(3)))
; DI bool moe_find(const Ctx& c, int qi, int NT, int& e, int& nt, int& mt, int& cn, int& hb) {
;     LAS int* S = (LAS int*)(c.lds + MS_OFF);
;     const int nown = __builtin_amdgcn_readfirstlane(S[0]); int accu = 0;
;     for (int k = 0; k < nown; ++k) { const int mc = __builtin_amdgcn_readfirstlane(S[9 + 4 * k]);
;         if (qi < accu + NT * mc) { const int loc = qi - accu; nt = loc / mc; mt = loc - nt * mc;
;             e = __builtin_amdgcn_readfirstlane(S[8 + 4 * k]); cn = __builtin_amdgcn_readfirstlane(S[10 + 4 * k]); hb = __builtin_amdgcn_readfirstlane(S[11 + 4 * k]); return true; }
;         accu += NT * mc; }
.LBB0_653:
	v_mov_b32_e32 v176, s5
	ds_read_b32 v176, v176
	s_add_i32 s92, s92, 1
	s_waitcnt lgkmcnt(0)
	v_readfirstlane_b32 s16, v176
	s_cmp_lt_i32 s16, 1
	s_cbranch_scc1 .LBB0_660
	s_mul_i32 s25, s92, s70
	s_add_i32 s16, s16, -1
	s_add_i32 s100, s33, s92
	s_and_b32 s100, s100, 31
	s_cmp_eq_u32 s70, 32
	s_cselect_b32 s100, s100, s33
	s_add_i32 s25, s25, s100
	s_mov_b32 s27, 0
	v_mov_b32_e32 v176, s16
	s_mov_b32 s26, s52

; DI int lane_id() { int l; asm volatile("v_mbcnt_lo_u32_b32 %0, -1, 0\n\tv_mbcnt_hi_u32_b32 %0, -1, %0" : "=v"(l)); return l; }
; #define G_SETUP_B(u) do { rsB0 = mk_rsrc((u).b0); rsB1 = mk_rsrc((u).b1); } while (0)
; #define G_ENDTILE(VM) do { asm volatile("s_waitcnt vmcnt(" #VM ")" ::: "memory"); \
;         asm volatile("s_waitcnt lgkmcnt(0)" ::: "memory"); __builtin_amdgcn_s_barrier(); asm volatile("" ::: "memory"); } while (0)
;     ...
;         U nxt = cur;
;         const bool has_next = sched.get(ui + 1, nxt);
;         G_SETUP_B(nxt);
;         G_TILE(G_A0, G_B0, true, G_B1, G_A1, nt - 1, true, 0, G_SETUP_A(nxt));
;         G_ENDTILE(8);
;         G_TILE(G_A1, G_B1, true, G_B0, G_A0, 0, true, 1, (void)0);
;         G_ENDTILE(8);
;         { const int l2 = lane_id(); cur.ep(acc, wr, wc, l2 & 15, l2 >> 4); }
;         if (!has_next) break;
;         cur = nxt;
.LBB0_661:
	s_xor_b64 s[30:31], s[16:17], -1
	s_andn2_b64 vcc, exec, s[16:17]
	s_mov_b32 s42, s54
	s_mov_b32 s43, s68
	s_mov_b64 s[62:63], s[58:59]
	s_mov_b64 s[60:61], s[56:57]
	s_cbranch_vccnz .LBB0_648
	s_lshl_b32 s16, s24, 13
	s_ashr_i32 s17, s16, 31
	s_lshl_b64 s[16:17], s[16:17], 2
	s_add_u32 s66, s74, s16
	s_addc_u32 s67, s75, s17
	s_ashr_i32 s25, s24, 31
	s_lshl_b64 s[16:17], s[24:25], 24
	s_add_u32 s25, s8, s16
	s_addc_u32 s38, s9, s17
	s_or_b32 s42, s27, s76
	s_ashr_i32 s43, s42, 31
	s_lshl_b64 s[36:37], s[42:43], 2
	s_add_u32 s55, s25, s36
	s_addc_u32 s77, s38, s37
	s_add_u32 s16, s12, s16
	s_addc_u32 s17, s13, s17
	s_add_u32 s79, s16, s36
	s_addc_u32 s80, s17, s37
	s_lshl_b32 s16, s24, 11
	s_ashr_i32 s17, s16, 31
	s_lshl_b64 s[16:17], s[16:17], 2
	s_add_u32 s60, s10, s16
	s_addc_u32 s61, s11, s17
	s_add_u32 s62, s14, s16
	s_addc_u32 s63, s15, s17
	s_add_i32 s43, s29, s26
	s_mov_b32 s65, s28
	s_mov_b32 s78, s26
	s_mul_i32 s100, s72, 0x90
	s_sub_i32 s99, s28, s26
	s_sub_i32 s99, s99, s100
	s_add_i32 s99, s99, 15
	s_max_i32 s99, s99, 0
	s_lshr_b32 s99, s99, 4
	s_min_u32 s99, s99, 9
	s_branch .LBB0_648

.LBB0_854:
	s_lshl_b32 s42, s8, 8
	s_mul_i32 s96, s9, 0x120
	s_mul_i32 s100, s72, 0x90
	s_sub_i32 s99, s6, s96
	s_sub_i32 s99, s99, s100
	s_add_i32 s99, s99, 15
	s_max_i32 s99, s99, 0
	s_lshr_b32 s99, s99, 4
	s_min_u32 s99, s99, 9
	s_branch .LBB0_856

;     ...
;         for (int m = 0; m < MF; ++m)
; #pragma unroll
;             for (int n = 0; n < 4; ++n) acc[m][n] = (f32x4){0.f, 0.f, 0.f, 0.f};
;         for (int t = 0; t < nt - 2; t += 2) {
.LBB0_861:
	s_andn2_b64 vcc, exec, s[28:29]
	v_mov_b32_e32 v175, 0
	s_cbranch_vccnz .LBB0_864
	v_mov_b32_e32 v32, 0
	s_mov_b32 s8, 0
	s_mov_b32 s9, 0x1e0000
	s_movk_i32 s36, 0x100
	v_mov_b32_e32 v33, v32
	v_mov_b32_e32 v34, v32
	v_mov_b32_e32 v35, v32
	v_mov_b32_e32 v36, v32
	v_mov_b32_e32 v37, v32
	v_mov_b32_e32 v38, v32
	v_mov_b32_e32 v39, v32
	v_mov_b32_e32 v40, v32
	v_mov_b32_e32 v41, v32
	v_mov_b32_e32 v42, v32
	v_mov_b32_e32 v43, v32
	s_waitcnt vmcnt(1)
	v_mov_b32_e32 v44, v32
	v_mov_b32_e32 v45, v32
	v_mov_b32_e32 v46, v32
	v_mov_b32_e32 v47, v32
	v_mov_b32_e32 v48, v32
	v_mov_b32_e32 v49, v32
	v_mov_b32_e32 v50, v32
	v_mov_b32_e32 v51, v32
	s_waitcnt vmcnt(0)
	v_mov_b32_e32 v52, v32
	v_mov_b32_e32 v53, v32
	v_mov_b32_e32 v54, v32
	v_mov_b32_e32 v55, v32
	v_mov_b32_e32 v56, v32
	v_mov_b32_e32 v57, v32
	v_mov_b32_e32 v58, v32
	v_mov_b32_e32 v59, v32
	v_mov_b32_e32 v68, v32
	v_mov_b32_e32 v69, v32
	v_mov_b32_e32 v70, v32
	v_mov_b32_e32 v71, v32
	v_mov_b32_e32 v76, v32
	v_mov_b32_e32 v77, v32
	v_mov_b32_e32 v78, v32
	v_mov_b32_e32 v79, v32
	v_mov_b32_e32 v60, v32
	v_mov_b32_e32 v61, v32
	v_mov_b32_e32 v62, v32
	v_mov_b32_e32 v63, v32
	v_mov_b32_e32 v64, v32
	v_mov_b32_e32 v65, v32
	v_mov_b32_e32 v66, v32
	v_mov_b32_e32 v67, v32
	v_mov_b32_e32 v72, v32
	v_mov_b32_e32 v73, v32
	v_mov_b32_e32 v74, v32
	v_mov_b32_e32 v75, v32
	v_mov_b32_e32 v80, v32
	v_mov_b32_e32 v81, v32
	v_mov_b32_e32 v82, v32
	v_mov_b32_e32 v83, v32
	v_mov_b32_e32 v84, v32
	v_mov_b32_e32 v85, v32
	v_mov_b32_e32 v86, v32
	v_mov_b32_e32 v87, v32
	v_mov_b32_e32 v96, v32
	v_mov_b32_e32 v97, v32
	v_mov_b32_e32 v98, v32
	v_mov_b32_e32 v99, v32
	v_mov_b32_e32 v104, v32
	v_mov_b32_e32 v105, v32
	v_mov_b32_e32 v106, v32
	v_mov_b32_e32 v107, v32
	v_mov_b32_e32 v108, v32
	v_mov_b32_e32 v109, v32
	v_mov_b32_e32 v110, v32
	v_mov_b32_e32 v111, v32
	v_mov_b32_e32 v88, v32
	v_mov_b32_e32 v89, v32
	v_mov_b32_e32 v90, v32
	v_mov_b32_e32 v91, v32
	v_mov_b32_e32 v92, v32
	v_mov_b32_e32 v93, v32
	v_mov_b32_e32 v94, v32
	v_mov_b32_e32 v95, v32
	v_mov_b32_e32 v100, v32
	v_mov_b32_e32 v101, v32
	v_mov_b32_e32 v102, v32
	v_mov_b32_e32 v103, v32
	v_mov_b32_e32 v112, v32
	v_mov_b32_e32 v113, v32
	v_mov_b32_e32 v114, v32
	v_mov_b32_e32 v115, v32
	v_mov_b32_e32 v116, v32
	v_mov_b32_e32 v117, v32
	v_mov_b32_e32 v118, v32
	v_mov_b32_e32 v119, v32
	v_mov_b32_e32 v128, v32
	v_mov_b32_e32 v129, v32
	v_mov_b32_e32 v130, v32
	v_mov_b32_e32 v131, v32
	v_mov_b32_e32 v136, v32
	v_mov_b32_e32 v137, v32
	v_mov_b32_e32 v138, v32
	v_mov_b32_e32 v139, v32
	v_mov_b32_e32 v140, v32
	v_mov_b32_e32 v141, v32
	v_mov_b32_e32 v142, v32
	v_mov_b32_e32 v143, v32
	v_mov_b32_e32 v120, v32
	v_mov_b32_e32 v121, v32
	v_mov_b32_e32 v122, v32
	v_mov_b32_e32 v123, v32
	v_mov_b32_e32 v124, v32
	v_mov_b32_e32 v125, v32
	v_mov_b32_e32 v126, v32
	v_mov_b32_e32 v127, v32
	v_mov_b32_e32 v132, v32
	v_mov_b32_e32 v133, v32
	v_mov_b32_e32 v134, v32
	v_mov_b32_e32 v135, v32
	v_mov_b32_e32 v144, v32
	v_mov_b32_e32 v145, v32
	v_mov_b32_e32 v146, v32
	v_mov_b32_e32 v147, v32
	v_mov_b32_e32 v148, v32
	v_mov_b32_e32 v149, v32
	v_mov_b32_e32 v150, v32
	v_mov_b32_e32 v151, v32
	v_mov_b32_e32 v152, v32
	v_mov_b32_e32 v153, v32
	v_mov_b32_e32 v154, v32
	v_mov_b32_e32 v155, v32
	v_mov_b32_e32 v156, v32
	v_mov_b32_e32 v157, v32
	v_mov_b32_e32 v158, v32
	v_mov_b32_e32 v159, v32
	v_mov_b32_e32 v160, v32
	v_mov_b32_e32 v161, v32
	v_mov_b32_e32 v162, v32
	v_mov_b32_e32 v163, v32
	v_mov_b32_e32 v164, v32
	v_mov_b32_e32 v165, v32
	v_mov_b32_e32 v166, v32
	v_mov_b32_e32 v167, v32
	v_mov_b32_e32 v168, v32
	v_mov_b32_e32 v169, v32
	v_mov_b32_e32 v170, v32
	v_mov_b32_e32 v171, v32
	v_mov_b32_e32 v172, v32
	v_mov_b32_e32 v173, v32
	v_mov_b32_e32 v174, v32
	v_mov_b32_e32 v175, v32
	v_mov_b32_e32 v216, 0
	v_mov_b32_e32 v217, 0
	v_mov_b32_e32 v218, 0
	v_mov_b32_e32 v219, 0
	v_mov_b32_e32 v220, 0
	v_mov_b32_e32 v221, 0
	v_mov_b32_e32 v222, 0
	v_mov_b32_e32 v223, 0
	v_mov_b32_e32 v244, 0
	v_mov_b32_e32 v245, 0
	v_mov_b32_e32 v246, 0
	v_mov_b32_e32 v247, 0
	v_mov_b32_e32 v248, 0
	v_mov_b32_e32 v249, 0
	v_mov_b32_e32 v250, 0
	v_mov_b32_e32 v251, 0
	v_mov_b32_e32 v252, 0
	v_mov_b32_e32 v253, 0
	v_mov_b32_e32 v254, 0
	v_mov_b32_e32 v255, 0
	s_cmp_lt_u32 s99, 9
	s_cbranch_scc1 .Lchk6_loop

.Lchk6_loop:
	s_mov_b32 m0, s85
	s_add_i32 s38, s36, 0xffffff80
	ds_read_b64_tr_b16 v[178:179], v206
	ds_read_b64_tr_b16 v[176:177], v205
	ds_read_b64_tr_b16 v[180:181], v205 offset:32
	ds_read_b64_tr_b16 v[184:185], v205 offset:64
	ds_read_b64_tr_b16 v[188:189], v205 offset:96
	ds_read_b128 v[192:195], v199
	ds_read_b64_tr_b16 v[182:183], v206 offset:32
	ds_read_b64_tr_b16 v[186:187], v206 offset:64
	ds_read_b64_tr_b16 v[190:191], v206 offset:96
	ds_read_b128 v[208:211], v199 offset:2048
	ds_read_b128 v[212:215], v199 offset:4096
	buffer_load_dwordx4 v200, s[20:23], s38 offen lds
	s_mov_b32 m0, s86
	s_cmp_le_u32 s99, 8
	s_cbranch_scc1 .Lchk6_s1
	v_mfma_f32_16x16x32_bf16 v[44:47], v[244:247], v[252:255], v[44:47]
	v_mfma_f32_16x16x32_bf16 v[40:43], v[248:251], v[252:255], v[40:43]
	v_mfma_f32_16x16x32_bf16 v[36:39], v[216:219], v[252:255], v[36:39]
	v_mfma_f32_16x16x32_bf16 v[32:35], v[220:223], v[252:255], v[32:35]
.Lchk6_s1:
	s_waitcnt lgkmcnt(0)
	s_cmp_le_u32 s99, 0
	s_cbranch_scc1 .Lchk6_s2
	v_mfma_f32_16x16x32_bf16 v[172:175], v[176:179], v[192:195], v[172:175]
	v_mfma_f32_16x16x32_bf16 v[168:171], v[180:183], v[192:195], v[168:171]
	v_mfma_f32_16x16x32_bf16 v[164:167], v[184:187], v[192:195], v[164:167]
	v_mfma_f32_16x16x32_bf16 v[160:163], v[188:191], v[192:195], v[160:163]
.Lchk6_s2:
	buffer_load_dwordx4 v201, s[20:23], s38 offen lds
	s_mov_b32 m0, s87
	s_nop 0
	buffer_load_dwordx4 v202, s[20:23], s38 offen lds
	s_mov_b32 m0, s88
	s_nop 0
	buffer_load_dwordx4 v203, s[20:23], s38 offen lds
	s_mov_b32 m0, s89
	s_nop 0
	buffer_load_dwordx4 v204, s[20:23], s38 offen lds
	s_add_i32 s38, s9, 0xfff20000
	s_waitcnt vmcnt(12)
	s_cmp_le_u32 s99, 1
	s_cbranch_scc1 .Lchk6_s3
	v_mfma_f32_16x16x32_bf16 v[156:159], v[176:179], v[208:211], v[156:159]
	v_mfma_f32_16x16x32_bf16 v[152:155], v[180:183], v[208:211], v[152:155]
	v_mfma_f32_16x16x32_bf16 v[148:151], v[184:187], v[208:211], v[148:151]
	v_mfma_f32_16x16x32_bf16 v[144:147], v[188:191], v[208:211], v[144:147]
.Lchk6_s3:
	ds_read_b128 v[192:195], v199 offset:6144
	v_cvt_pk_bf16_f32 v23, v22, v23
	v_cvt_pk_bf16_f32 v22, v20, v21
	ds_write_b64 v198, v[22:23] offset:34816
	buffer_load_dwordx4 v[20:23], v197, s[24:27], s38 offen
	s_cmp_le_u32 s99, 2
	s_cbranch_scc1 .Lchk6_s4
	v_mfma_f32_16x16x32_bf16 v[132:135], v[176:179], v[212:215], v[132:135]
	v_mfma_f32_16x16x32_bf16 v[124:127], v[180:183], v[212:215], v[124:127]
	v_mfma_f32_16x16x32_bf16 v[120:123], v[184:187], v[212:215], v[120:123]
	v_mfma_f32_16x16x32_bf16 v[140:143], v[188:191], v[212:215], v[140:143]
.Lchk6_s4:
	ds_read_b128 v[208:211], v199 offset:8192
	s_waitcnt lgkmcnt(2)
	s_waitcnt vmcnt(11)
	s_cmp_le_u32 s99, 3
	s_cbranch_scc1 .Lchk6_s5
	v_mfma_f32_16x16x32_bf16 v[136:139], v[176:179], v[192:195], v[136:139]
	v_mfma_f32_16x16x32_bf16 v[128:131], v[180:183], v[192:195], v[128:131]
	v_mfma_f32_16x16x32_bf16 v[116:119], v[184:187], v[192:195], v[116:119]
	v_mfma_f32_16x16x32_bf16 v[112:115], v[188:191], v[192:195], v[112:115]
.Lchk6_s5:
	ds_read_b128 v[212:215], v199 offset:10240
	v_cvt_pk_bf16_f32 v31, v30, v31
	v_cvt_pk_bf16_f32 v30, v28, v29
	ds_write_b64 v198, v[30:31] offset:43520
	s_add_i32 s39, s9, 0xfff40000
	buffer_load_dwordx4 v[28:31], v197, s[24:27], s39 offen
	s_waitcnt lgkmcnt(2)
	s_cmp_le_u32 s99, 4
	s_cbranch_scc1 .Lchk6_s6
	v_mfma_f32_16x16x32_bf16 v[100:103], v[176:179], v[208:211], v[100:103]
	v_mfma_f32_16x16x32_bf16 v[92:95], v[180:183], v[208:211], v[92:95]
	v_mfma_f32_16x16x32_bf16 v[88:91], v[184:187], v[208:211], v[88:91]
	v_mfma_f32_16x16x32_bf16 v[108:111], v[188:191], v[208:211], v[108:111]
.Lchk6_s6:
	ds_read_b128 v[192:195], v199 offset:12288
	s_waitcnt lgkmcnt(2)
	s_cmp_le_u32 s99, 5
	s_cbranch_scc1 .Lchk6_s7
	v_mfma_f32_16x16x32_bf16 v[104:107], v[176:179], v[212:215], v[104:107]
	v_mfma_f32_16x16x32_bf16 v[96:99], v[180:183], v[212:215], v[96:99]
	v_mfma_f32_16x16x32_bf16 v[84:87], v[184:187], v[212:215], v[84:87]
	v_mfma_f32_16x16x32_bf16 v[80:83], v[188:191], v[212:215], v[80:83]
.Lchk6_s7:
	ds_read_b128 v[208:211], v199 offset:14336
	v_cvt_pk_bf16_f32 v19, v18, v19
	v_cvt_pk_bf16_f32 v18, v16, v17
	ds_write_b64 v198, v[18:19] offset:52224
	s_add_i32 s43, s9, 0xfff60000
	buffer_load_dwordx4 v[16:19], v197, s[24:27], s43 offen
	s_waitcnt lgkmcnt(2)
	s_cmp_le_u32 s99, 6
	s_cbranch_scc1 .Lchk6_s8
	v_mfma_f32_16x16x32_bf16 v[72:75], v[176:179], v[192:195], v[72:75]
	v_mfma_f32_16x16x32_bf16 v[64:67], v[180:183], v[192:195], v[64:67]
	v_mfma_f32_16x16x32_bf16 v[60:63], v[184:187], v[192:195], v[60:63]
	v_mfma_f32_16x16x32_bf16 v[76:79], v[188:191], v[192:195], v[76:79]
.Lchk6_s8:
	ds_read_b128 v[212:215], v199 offset:16384
	s_waitcnt lgkmcnt(2)
	s_waitcnt vmcnt(12)
	s_cmp_le_u32 s99, 7
	s_cbranch_scc1 .Lchk6_s9
	v_mfma_f32_16x16x32_bf16 v[68:71], v[176:179], v[208:211], v[68:71]
	v_mfma_f32_16x16x32_bf16 v[56:59], v[180:183], v[208:211], v[56:59]
	v_mfma_f32_16x16x32_bf16 v[52:55], v[184:187], v[208:211], v[52:55]
	v_mfma_f32_16x16x32_bf16 v[48:51], v[188:191], v[208:211], v[48:51]
.Lchk6_s9:
	ds_read_b128 v[192:195], v199 offset:1024
	v_cvt_pk_bf16_f32 v27, v26, v27
	v_cvt_pk_bf16_f32 v26, v24, v25
	ds_write_b64 v198, v[26:27] offset:60928
	s_add_i32 s45, s9, 0xfff80000
	buffer_load_dwordx4 v[24:27], v197, s[24:27], s45 offen
	ds_read_b128 v[208:211], v199 offset:3072
	s_waitcnt lgkmcnt(3)
	s_cmp_le_u32 s99, 8
	s_cbranch_scc1 .Lchk6_s10
	v_mfma_f32_16x16x32_bf16 v[44:47], v[176:179], v[212:215], v[44:47]
	v_mfma_f32_16x16x32_bf16 v[40:43], v[180:183], v[212:215], v[40:43]
	v_mfma_f32_16x16x32_bf16 v[36:39], v[184:187], v[212:215], v[36:39]
	v_mfma_f32_16x16x32_bf16 v[32:35], v[188:191], v[212:215], v[32:35]
.Lchk6_s10:
	ds_read_b64_tr_b16 v[246:247], v206 offset:17408
	ds_read_b64_tr_b16 v[218:219], v206 offset:17440
	ds_read_b64_tr_b16 v[244:245], v205 offset:17408
	ds_read_b64_tr_b16 v[216:217], v205 offset:17440
	ds_read_b64_tr_b16 v[248:249], v205 offset:17472
	ds_read_b64_tr_b16 v[250:251], v206 offset:17472
	ds_read_b64_tr_b16 v[252:253], v205 offset:17504
	ds_read_b64_tr_b16 v[254:255], v206 offset:17504
	s_waitcnt lgkmcnt(5)
	s_waitcnt vmcnt(12)
	s_waitcnt lgkmcnt(4)
	s_waitcnt lgkmcnt(2)
	s_waitcnt lgkmcnt(0)
	s_cmp_le_u32 s99, 0
	s_cbranch_scc1 .Lchk6_s11
	v_mfma_f32_16x16x32_bf16 v[172:175], v[244:247], v[192:195], v[172:175]
	v_mfma_f32_16x16x32_bf16 v[168:171], v[216:219], v[192:195], v[168:171]
	v_mfma_f32_16x16x32_bf16 v[164:167], v[248:251], v[192:195], v[164:167]
	v_mfma_f32_16x16x32_bf16 v[160:163], v[252:255], v[192:195], v[160:163]
.Lchk6_s11:
	ds_read_b128 v[188:191], v199 offset:5120
	v_cvt_pk_bf16_f32 v15, v14, v15
	v_cvt_pk_bf16_f32 v14, v12, v13
	ds_write_b64 v198, v[14:15] offset:35072
	buffer_load_dwordx4 v[12:15], v197, s[16:19], s38 offen
	s_cmp_le_u32 s99, 1
	s_cbranch_scc1 .Lchk6_s12
	v_mfma_f32_16x16x32_bf16 v[156:159], v[244:247], v[208:211], v[156:159]
	v_mfma_f32_16x16x32_bf16 v[152:155], v[216:219], v[208:211], v[152:155]
	v_mfma_f32_16x16x32_bf16 v[148:151], v[248:251], v[208:211], v[148:151]
	v_mfma_f32_16x16x32_bf16 v[144:147], v[252:255], v[208:211], v[144:147]
.Lchk6_s12:
	ds_read_b128 v[192:195], v199 offset:7168
	s_waitcnt lgkmcnt(2)
	s_waitcnt vmcnt(11)
	s_cmp_le_u32 s99, 2
	s_cbranch_scc1 .Lchk6_s13
	v_mfma_f32_16x16x32_bf16 v[132:135], v[244:247], v[188:191], v[132:135]
	v_mfma_f32_16x16x32_bf16 v[124:127], v[216:219], v[188:191], v[124:127]
	v_mfma_f32_16x16x32_bf16 v[120:123], v[248:251], v[188:191], v[120:123]
	v_mfma_f32_16x16x32_bf16 v[140:143], v[252:255], v[188:191], v[140:143]
.Lchk6_s13:
	ds_read_b128 v[208:211], v199 offset:9216
	v_cvt_pk_bf16_f32 v7, v6, v7
	v_cvt_pk_bf16_f32 v6, v4, v5
	ds_write_b64 v198, v[6:7] offset:43776
	buffer_load_dwordx4 v[4:7], v197, s[16:19], s39 offen
	s_waitcnt lgkmcnt(2)
	s_cmp_le_u32 s99, 3
	s_cbranch_scc1 .Lchk6_s14
	v_mfma_f32_16x16x32_bf16 v[136:139], v[244:247], v[192:195], v[136:139]
	v_mfma_f32_16x16x32_bf16 v[128:131], v[216:219], v[192:195], v[128:131]
	v_mfma_f32_16x16x32_bf16 v[116:119], v[248:251], v[192:195], v[116:119]
	v_mfma_f32_16x16x32_bf16 v[112:115], v[252:255], v[192:195], v[112:115]
.Lchk6_s14:
	ds_read_b128 v[188:191], v199 offset:11264
	s_waitcnt lgkmcnt(2)
	s_cmp_le_u32 s99, 4
	s_cbranch_scc1 .Lchk6_s15
	v_mfma_f32_16x16x32_bf16 v[100:103], v[244:247], v[208:211], v[100:103]
	v_mfma_f32_16x16x32_bf16 v[92:95], v[216:219], v[208:211], v[92:95]
	v_mfma_f32_16x16x32_bf16 v[88:91], v[248:251], v[208:211], v[88:91]
	v_mfma_f32_16x16x32_bf16 v[108:111], v[252:255], v[208:211], v[108:111]
.Lchk6_s15:
	ds_read_b128 v[192:195], v199 offset:13312
	v_cvt_pk_bf16_f32 v3, v2, v3
	v_cvt_pk_bf16_f32 v2, v0, v1
	ds_write_b64 v198, v[2:3] offset:52480
	buffer_load_dwordx4 v[0:3], v197, s[16:19], s43 offen
	s_waitcnt lgkmcnt(2)
	s_cmp_le_u32 s99, 5
	s_cbranch_scc1 .Lchk6_s16
	v_mfma_f32_16x16x32_bf16 v[104:107], v[244:247], v[188:191], v[104:107]
	v_mfma_f32_16x16x32_bf16 v[96:99], v[216:219], v[188:191], v[96:99]
	v_mfma_f32_16x16x32_bf16 v[84:87], v[248:251], v[188:191], v[84:87]
	v_mfma_f32_16x16x32_bf16 v[80:83], v[252:255], v[188:191], v[80:83]
.Lchk6_s16:
	ds_read_b128 v[208:211], v199 offset:15360
	s_waitcnt lgkmcnt(2)
	s_waitcnt vmcnt(12)
	s_cmp_le_u32 s99, 6
	s_cbranch_scc1 .Lchk6_s17
	v_mfma_f32_16x16x32_bf16 v[72:75], v[244:247], v[192:195], v[72:75]
	v_mfma_f32_16x16x32_bf16 v[64:67], v[216:219], v[192:195], v[64:67]
	v_mfma_f32_16x16x32_bf16 v[60:63], v[248:251], v[192:195], v[60:63]
	v_mfma_f32_16x16x32_bf16 v[76:79], v[252:255], v[192:195], v[76:79]
.Lchk6_s17:
	ds_read_b128 v[236:239], v199 offset:17408
	v_cvt_pk_bf16_f32 v11, v10, v11
	v_cvt_pk_bf16_f32 v10, v8, v9
	ds_write_b64 v198, v[10:11] offset:61184
	buffer_load_dwordx4 v[8:11], v197, s[16:19], s45 offen
	s_waitcnt lgkmcnt(2)
	s_cmp_le_u32 s99, 7
	s_cbranch_scc1 .Lchk6_s18
	v_mfma_f32_16x16x32_bf16 v[68:71], v[244:247], v[208:211], v[68:71]
	v_mfma_f32_16x16x32_bf16 v[56:59], v[216:219], v[208:211], v[56:59]
	v_mfma_f32_16x16x32_bf16 v[52:55], v[248:251], v[208:211], v[52:55]
	v_mfma_f32_16x16x32_bf16 v[48:51], v[252:255], v[208:211], v[48:51]
.Lchk6_s18:
	s_waitcnt lgkmcnt(1)
	s_waitcnt vmcnt(8)
	s_mov_b32 m0, s49
	s_waitcnt lgkmcnt(0)
	s_barrier
	ds_read_b64_tr_b16 v[178:179], v206 offset:34816
	ds_read_b64_tr_b16 v[176:177], v205 offset:34816
	ds_read_b64_tr_b16 v[180:181], v205 offset:34848
	ds_read_b64_tr_b16 v[184:185], v205 offset:34880
	ds_read_b64_tr_b16 v[188:189], v205 offset:34912
	ds_read_b128 v[192:195], v199 offset:36864
	ds_read_b64_tr_b16 v[182:183], v206 offset:34848
	ds_read_b64_tr_b16 v[186:187], v206 offset:34880
	ds_read_b64_tr_b16 v[190:191], v206 offset:34912
	ds_read_b128 v[208:211], v199 offset:38912
	ds_read_b128 v[212:215], v199 offset:40960
	buffer_load_dwordx4 v200, s[20:23], s36 offen lds
	s_mov_b32 m0, s68
	s_cmp_le_u32 s99, 8
	s_cbranch_scc1 .Lchk6_s19
	v_mfma_f32_16x16x32_bf16 v[44:47], v[244:247], v[236:239], v[44:47]
	v_mfma_f32_16x16x32_bf16 v[40:43], v[216:219], v[236:239], v[40:43]
	v_mfma_f32_16x16x32_bf16 v[36:39], v[248:251], v[236:239], v[36:39]
	v_mfma_f32_16x16x32_bf16 v[32:35], v[252:255], v[236:239], v[32:35]
.Lchk6_s19:
	s_waitcnt lgkmcnt(5)
	s_waitcnt lgkmcnt(4)
	s_waitcnt lgkmcnt(3)
	s_waitcnt lgkmcnt(2)
	s_cmp_le_u32 s99, 0
	s_cbranch_scc1 .Lchk6_s20
	v_mfma_f32_16x16x32_bf16 v[172:175], v[176:179], v[192:195], v[172:175]
	v_mfma_f32_16x16x32_bf16 v[168:171], v[180:183], v[192:195], v[168:171]
	v_mfma_f32_16x16x32_bf16 v[164:167], v[184:187], v[192:195], v[164:167]
	v_mfma_f32_16x16x32_bf16 v[160:163], v[188:191], v[192:195], v[160:163]
.Lchk6_s20:
	buffer_load_dwordx4 v201, s[20:23], s36 offen lds
	s_mov_b32 m0, s77
	s_add_i32 s38, s9, 0xfffa0000
	buffer_load_dwordx4 v202, s[20:23], s36 offen lds
	s_mov_b32 m0, s78
	s_nop 0
	buffer_load_dwordx4 v203, s[20:23], s36 offen lds
	s_mov_b32 m0, s79
	s_nop 0
	buffer_load_dwordx4 v204, s[20:23], s36 offen lds
	s_waitcnt lgkmcnt(1)
	s_waitcnt vmcnt(12)
	s_cmp_le_u32 s99, 1
	s_cbranch_scc1 .Lchk6_s21
	v_mfma_f32_16x16x32_bf16 v[156:159], v[176:179], v[208:211], v[156:159]
	v_mfma_f32_16x16x32_bf16 v[152:155], v[180:183], v[208:211], v[152:155]
	v_mfma_f32_16x16x32_bf16 v[148:151], v[184:187], v[208:211], v[148:151]
	v_mfma_f32_16x16x32_bf16 v[144:147], v[188:191], v[208:211], v[144:147]
.Lchk6_s21:
	ds_read_b128 v[192:195], v199 offset:43008
	v_cvt_pk_bf16_f32 v23, v22, v23
	v_cvt_pk_bf16_f32 v22, v20, v21
	ds_write_b64 v198, v[22:23]
	buffer_load_dwordx4 v[20:23], v197, s[24:27], s38 offen
	s_waitcnt lgkmcnt(2)
	s_cmp_le_u32 s99, 2
	s_cbranch_scc1 .Lchk6_s22
	v_mfma_f32_16x16x32_bf16 v[132:135], v[176:179], v[212:215], v[132:135]
	v_mfma_f32_16x16x32_bf16 v[124:127], v[180:183], v[212:215], v[124:127]
	v_mfma_f32_16x16x32_bf16 v[120:123], v[184:187], v[212:215], v[120:123]
	v_mfma_f32_16x16x32_bf16 v[140:143], v[188:191], v[212:215], v[140:143]
.Lchk6_s22:
	ds_read_b128 v[208:211], v199 offset:45056
	s_waitcnt lgkmcnt(2)
	s_waitcnt vmcnt(12)
	s_cmp_le_u32 s99, 3
	s_cbranch_scc1 .Lchk6_s23
	v_mfma_f32_16x16x32_bf16 v[136:139], v[176:179], v[192:195], v[136:139]
	v_mfma_f32_16x16x32_bf16 v[128:131], v[180:183], v[192:195], v[128:131]
	v_mfma_f32_16x16x32_bf16 v[116:119], v[184:187], v[192:195], v[116:119]
	v_mfma_f32_16x16x32_bf16 v[112:115], v[188:191], v[192:195], v[112:115]
.Lchk6_s23:
	ds_read_b128 v[212:215], v199 offset:47104
	v_cvt_pk_bf16_f32 v31, v30, v31
	v_cvt_pk_bf16_f32 v30, v28, v29
	ds_write_b64 v198, v[30:31] offset:8704
	s_add_i32 s39, s9, 0xfffc0000
	buffer_load_dwordx4 v[28:31], v197, s[24:27], s39 offen
	s_waitcnt lgkmcnt(2)
	s_cmp_le_u32 s99, 4
	s_cbranch_scc1 .Lchk6_s24
	v_mfma_f32_16x16x32_bf16 v[100:103], v[176:179], v[208:211], v[100:103]
	v_mfma_f32_16x16x32_bf16 v[92:95], v[180:183], v[208:211], v[92:95]
	v_mfma_f32_16x16x32_bf16 v[88:91], v[184:187], v[208:211], v[88:91]
	v_mfma_f32_16x16x32_bf16 v[108:111], v[188:191], v[208:211], v[108:111]
.Lchk6_s24:
	ds_read_b128 v[192:195], v199 offset:49152
	s_waitcnt lgkmcnt(2)
	s_waitcnt vmcnt(12)
	s_cmp_le_u32 s99, 5
	s_cbranch_scc1 .Lchk6_s25
	v_mfma_f32_16x16x32_bf16 v[104:107], v[176:179], v[212:215], v[104:107]
	v_mfma_f32_16x16x32_bf16 v[96:99], v[180:183], v[212:215], v[96:99]
	v_mfma_f32_16x16x32_bf16 v[84:87], v[184:187], v[212:215], v[84:87]
	v_mfma_f32_16x16x32_bf16 v[80:83], v[188:191], v[212:215], v[80:83]
.Lchk6_s25:
	ds_read_b128 v[208:211], v199 offset:51200
	v_cvt_pk_bf16_f32 v19, v18, v19
	v_cvt_pk_bf16_f32 v18, v16, v17
	ds_write_b64 v198, v[18:19] offset:17408
	s_add_i32 s43, s9, 0xfffe0000
	buffer_load_dwordx4 v[16:19], v197, s[24:27], s43 offen
	s_waitcnt lgkmcnt(2)
	s_cmp_le_u32 s99, 6
	s_cbranch_scc1 .Lchk6_s26
	v_mfma_f32_16x16x32_bf16 v[72:75], v[176:179], v[192:195], v[72:75]
	v_mfma_f32_16x16x32_bf16 v[64:67], v[180:183], v[192:195], v[64:67]
	v_mfma_f32_16x16x32_bf16 v[60:63], v[184:187], v[192:195], v[60:63]
	v_mfma_f32_16x16x32_bf16 v[76:79], v[188:191], v[192:195], v[76:79]
.Lchk6_s26:
	ds_read_b128 v[212:215], v199 offset:53248
	s_waitcnt lgkmcnt(2)
	s_waitcnt vmcnt(12)
	s_cmp_le_u32 s99, 7
	s_cbranch_scc1 .Lchk6_s27
	v_mfma_f32_16x16x32_bf16 v[68:71], v[176:179], v[208:211], v[68:71]
	v_mfma_f32_16x16x32_bf16 v[56:59], v[180:183], v[208:211], v[56:59]
	v_mfma_f32_16x16x32_bf16 v[52:55], v[184:187], v[208:211], v[52:55]
	v_mfma_f32_16x16x32_bf16 v[48:51], v[188:191], v[208:211], v[48:51]
.Lchk6_s27:
	ds_read_b128 v[192:195], v199 offset:37888
	v_cvt_pk_bf16_f32 v27, v26, v27
	v_cvt_pk_bf16_f32 v26, v24, v25
	ds_write_b64 v198, v[26:27] offset:26112
	buffer_load_dwordx4 v[24:27], v197, s[24:27], s9 offen
	s_waitcnt lgkmcnt(2)
	s_cmp_le_u32 s99, 8
	s_cbranch_scc1 .Lchk6_s28
	v_mfma_f32_16x16x32_bf16 v[44:47], v[176:179], v[212:215], v[44:47]
	v_mfma_f32_16x16x32_bf16 v[40:43], v[180:183], v[212:215], v[40:43]
	v_mfma_f32_16x16x32_bf16 v[36:39], v[184:187], v[212:215], v[36:39]
	v_mfma_f32_16x16x32_bf16 v[32:35], v[188:191], v[212:215], v[32:35]
; #define G_DMA_A(kt, AO) do { G_DMA1(kt, AO, 0); G_DMA1(kt, AO, 1); G_DMA1(kt, AO, 2); G_DMA1(kt, AO, 3); if (MF == 9) G_DMA5(kt, AO); } while (0)
; #define G_ISSUE_B(kt) do { const unsigned _sb = (unsigned)(kt) * 4u * kstepB; \
;         _Pragma("unroll") for (int _i = 0; _i < 8; ++_i) sb[_i] = bload16(_i < 4 ? rsB0 : rsB1, vob, _sb + (_i & 3) * kstepB); } while (0)
; #define G_WRITE_B(BO) do { \
;         _Pragma("unroll") for (int _i = 0; _i < 8; ++_i) *(LAS u32x2*)(b_wr + (BO) + (_i & 3) * (16 * G_BSTRIDE) + (_i >> 2) * SLAB1) = pack4(__builtin_bit_cast(f32x4, sb[_i])); } while (0)
; #define G_ENDTILE(VM) do { asm volatile("s_waitcnt vmcnt(" #VM ")" ::: "memory"); \
;         asm volatile("s_waitcnt lgkmcnt(0)" ::: "memory"); __builtin_amdgcn_s_barrier(); asm volatile("" ::: "memory"); } while (0)
;     ...
;     __builtin_amdgcn_s_barrier();
;     G_DMA_A(0, G_A0); G_ISSUE_B(0); G_WRITE_B(G_B0);
;     __builtin_amdgcn_sched_barrier(0);
;     G_ISSUE_B(1);
;     __builtin_amdgcn_sched_barrier(0);
;     G_ENDTILE(8);
;     for (int ui = 0;; ++ui) {
; #pragma unroll
;         for (int m = 0; m < MF; ++m)
; #pragma unroll
;             for (int n = 0; n < 4; ++n) acc[m][n] = (f32x4){0.f, 0.f, 0.f, 0.f};
;         for (int t = 0; t < nt - 2; t += 2) {
;             G_TILE(G_A0, G_B0, true, G_B1, G_A1, t + 1, true, t + 2, (void)0);
;             G_ENDTILE(8);
;             G_TILE(G_A1, G_B1, true, G_B0, G_A0, t + 2, true, t + 3, (void)0);
;             G_ENDTILE(8);
;         }
.Lchk6_s28:
	ds_read_b128 v[176:179], v199 offset:39936
	ds_read_b64_tr_b16 v[244:245], v205 offset:52224
	ds_read_b64_tr_b16 v[248:249], v205 offset:52256
	ds_read_b64_tr_b16 v[216:217], v205 offset:52288
	ds_read_b64_tr_b16 v[220:221], v205 offset:52320
	ds_read_b64_tr_b16 v[246:247], v206 offset:52224
	ds_read_b64_tr_b16 v[250:251], v206 offset:52256
	ds_read_b64_tr_b16 v[218:219], v206 offset:52288
	ds_read_b64_tr_b16 v[222:223], v206 offset:52320
	s_waitcnt lgkmcnt(3)
	s_waitcnt vmcnt(12)
	s_waitcnt lgkmcnt(2)
	s_waitcnt lgkmcnt(1)
	s_waitcnt lgkmcnt(0)
	s_cmp_le_u32 s99, 0
	s_cbranch_scc1 .Lchk6_s29
	v_mfma_f32_16x16x32_bf16 v[172:175], v[244:247], v[192:195], v[172:175]
	v_mfma_f32_16x16x32_bf16 v[168:171], v[248:251], v[192:195], v[168:171]
	v_mfma_f32_16x16x32_bf16 v[164:167], v[216:219], v[192:195], v[164:167]
	v_mfma_f32_16x16x32_bf16 v[160:163], v[220:223], v[192:195], v[160:163]
.Lchk6_s29:
	ds_read_b128 v[184:187], v199 offset:41984
	v_cvt_pk_bf16_f32 v15, v14, v15
	v_cvt_pk_bf16_f32 v14, v12, v13
	ds_write_b64 v198, v[14:15] offset:256
	buffer_load_dwordx4 v[12:15], v197, s[16:19], s38 offen
	s_cmp_le_u32 s99, 1
	s_cbranch_scc1 .Lchk6_s30
	v_mfma_f32_16x16x32_bf16 v[156:159], v[244:247], v[176:179], v[156:159]
	v_mfma_f32_16x16x32_bf16 v[152:155], v[248:251], v[176:179], v[152:155]
	v_mfma_f32_16x16x32_bf16 v[148:151], v[216:219], v[176:179], v[148:151]
	v_mfma_f32_16x16x32_bf16 v[144:147], v[220:223], v[176:179], v[144:147]
.Lchk6_s30:
	ds_read_b128 v[188:191], v199 offset:44032
	s_waitcnt lgkmcnt(2)
	s_waitcnt vmcnt(12)
	s_cmp_le_u32 s99, 2
	s_cbranch_scc1 .Lchk6_s31
	v_mfma_f32_16x16x32_bf16 v[132:135], v[244:247], v[184:187], v[132:135]
	v_mfma_f32_16x16x32_bf16 v[124:127], v[248:251], v[184:187], v[124:127]
	v_mfma_f32_16x16x32_bf16 v[120:123], v[216:219], v[184:187], v[120:123]
	v_mfma_f32_16x16x32_bf16 v[140:143], v[220:223], v[184:187], v[140:143]
.Lchk6_s31:
	ds_read_b128 v[176:179], v199 offset:46080
	v_cvt_pk_bf16_f32 v7, v6, v7
	v_cvt_pk_bf16_f32 v6, v4, v5
	ds_write_b64 v198, v[6:7] offset:8960
	buffer_load_dwordx4 v[4:7], v197, s[16:19], s39 offen
	s_waitcnt lgkmcnt(2)
	s_cmp_le_u32 s99, 3
	s_cbranch_scc1 .Lchk6_s32
	v_mfma_f32_16x16x32_bf16 v[136:139], v[244:247], v[188:191], v[136:139]
	v_mfma_f32_16x16x32_bf16 v[128:131], v[248:251], v[188:191], v[128:131]
	v_mfma_f32_16x16x32_bf16 v[116:119], v[216:219], v[188:191], v[116:119]
	v_mfma_f32_16x16x32_bf16 v[112:115], v[220:223], v[188:191], v[112:115]
.Lchk6_s32:
	ds_read_b128 v[184:187], v199 offset:48128
	s_waitcnt lgkmcnt(2)
	s_waitcnt vmcnt(12)
	s_cmp_le_u32 s99, 4
	s_cbranch_scc1 .Lchk6_s33
	v_mfma_f32_16x16x32_bf16 v[100:103], v[244:247], v[176:179], v[100:103]
	v_mfma_f32_16x16x32_bf16 v[92:95], v[248:251], v[176:179], v[92:95]
	v_mfma_f32_16x16x32_bf16 v[88:91], v[216:219], v[176:179], v[88:91]
	v_mfma_f32_16x16x32_bf16 v[108:111], v[220:223], v[176:179], v[108:111]
.Lchk6_s33:
	ds_read_b128 v[188:191], v199 offset:50176
	v_cvt_pk_bf16_f32 v3, v2, v3
	v_cvt_pk_bf16_f32 v2, v0, v1
	ds_write_b64 v198, v[2:3] offset:17664
	buffer_load_dwordx4 v[0:3], v197, s[16:19], s43 offen
	s_waitcnt lgkmcnt(2)
	s_cmp_le_u32 s99, 5
	s_cbranch_scc1 .Lchk6_s34
	v_mfma_f32_16x16x32_bf16 v[104:107], v[244:247], v[184:187], v[104:107]
	v_mfma_f32_16x16x32_bf16 v[96:99], v[248:251], v[184:187], v[96:99]
	v_mfma_f32_16x16x32_bf16 v[84:87], v[216:219], v[184:187], v[84:87]
	v_mfma_f32_16x16x32_bf16 v[80:83], v[220:223], v[184:187], v[80:83]
.Lchk6_s34:
	ds_read_b128 v[176:179], v199 offset:52224
	s_waitcnt lgkmcnt(2)
	s_waitcnt vmcnt(12)
	s_cmp_le_u32 s99, 6
	s_cbranch_scc1 .Lchk6_s35
	v_mfma_f32_16x16x32_bf16 v[72:75], v[244:247], v[188:191], v[72:75]
	v_mfma_f32_16x16x32_bf16 v[64:67], v[248:251], v[188:191], v[64:67]
	v_mfma_f32_16x16x32_bf16 v[60:63], v[216:219], v[188:191], v[60:63]
	v_mfma_f32_16x16x32_bf16 v[76:79], v[220:223], v[188:191], v[76:79]
.Lchk6_s35:
	ds_read_b128 v[252:255], v199 offset:54272
	v_cvt_pk_bf16_f32 v11, v10, v11
	v_cvt_pk_bf16_f32 v10, v8, v9
	ds_write_b64 v198, v[10:11] offset:26368
	buffer_load_dwordx4 v[8:11], v197, s[16:19], s9 offen
	s_waitcnt lgkmcnt(2)
	s_cmp_le_u32 s99, 7
	s_cbranch_scc1 .Lchk6_s36
	v_mfma_f32_16x16x32_bf16 v[68:71], v[244:247], v[176:179], v[68:71]
	v_mfma_f32_16x16x32_bf16 v[56:59], v[248:251], v[176:179], v[56:59]
	v_mfma_f32_16x16x32_bf16 v[52:55], v[216:219], v[176:179], v[52:55]
	v_mfma_f32_16x16x32_bf16 v[48:51], v[220:223], v[176:179], v[48:51]
.Lchk6_s36:
	s_waitcnt lgkmcnt(1)
	s_waitcnt vmcnt(8)
	s_waitcnt lgkmcnt(0)
	s_barrier
	s_add_i32 s8, s8, 2
	s_add_i32 s9, s9, 0x100000
	s_addk_i32 s36, 0x100
	s_cmp_ge_i32 s8, s84
	s_cbranch_scc0 .Lchk6_loop
	s_cmp_le_u32 s99, 8
	s_cbranch_scc1 .Lchk6_s37
	v_mfma_f32_16x16x32_bf16 v[44:47], v[244:247], v[252:255], v[44:47]
	v_mfma_f32_16x16x32_bf16 v[40:43], v[248:251], v[252:255], v[40:43]
	v_mfma_f32_16x16x32_bf16 v[36:39], v[216:219], v[252:255], v[36:39]
	v_mfma_f32_16x16x32_bf16 v[32:35], v[220:223], v[252:255], v[32:35]

; #define LAS __attribute__((address_space(3)))
; DI bool moe_find(const Ctx& c, int qi, int NT, int& e, int& nt, int& mt, int& cn, int& hb) {
;     LAS int* S = (LAS int*)(c.lds + MS_OFF);
;     const int nown = __builtin_amdgcn_readfirstlane(S[0]); int accu = 0;
;     for (int k = 0; k < nown; ++k) { const int mc = __builtin_amdgcn_readfirstlane(S[9 + 4 * k]);
;         if (qi < accu + NT * mc) { const int loc = qi - accu; nt = loc / mc; mt = loc - nt * mc;
;             e = __builtin_amdgcn_readfirstlane(S[8 + 4 * k]); cn = __builtin_amdgcn_readfirstlane(S[10 + 4 * k]); hb = __builtin_amdgcn_readfirstlane(S[11 + 4 * k]); return true; }
;         accu += NT * mc; }
.LBB0_865:
	v_mov_b32_e32 v176, s92
	ds_read_b32 v176, v176
	s_add_i32 s95, s95, 1
	s_waitcnt lgkmcnt(0)
	v_readfirstlane_b32 s8, v176
	s_cmp_lt_i32 s8, 1
	s_cbranch_scc1 .LBB0_872
	s_mul_i32 s9, s95, s70
	s_add_i32 s8, s8, -1
	s_add_i32 s100, s33, s95
	s_and_b32 s100, s100, 31
	s_cmp_eq_u32 s70, 32
	s_cselect_b32 s100, s100, s33
	s_add_i32 s9, s9, s100
	s_mov_b32 s24, 0
	v_mov_b32_e32 v176, s8
	s_mov_b32 s18, s93

; DI int lane_id() { int l; asm volatile("v_mbcnt_lo_u32_b32 %0, -1, 0\n\tv_mbcnt_hi_u32_b32 %0, -1, %0" : "=v"(l)); return l; }
; #define G_SETUP_B(u) do { rsB0 = mk_rsrc((u).b0); rsB1 = mk_rsrc((u).b1); } while (0)
; #define G_ENDTILE(VM) do { asm volatile("s_waitcnt vmcnt(" #VM ")" ::: "memory"); \
;         asm volatile("s_waitcnt lgkmcnt(0)" ::: "memory"); __builtin_amdgcn_s_barrier(); asm volatile("" ::: "memory"); } while (0)
;     ...
;         U nxt = cur;
;         const bool has_next = sched.get(ui + 1, nxt);
;         G_SETUP_B(nxt);
;         G_TILE(G_A0, G_B0, true, G_B1, G_A1, nt - 1, true, 0, G_SETUP_A(nxt));
;         G_ENDTILE(8);
;         G_TILE(G_A1, G_B1, true, G_B0, G_A0, 0, true, 1, (void)0);
;         G_ENDTILE(8);
;         { const int l2 = lane_id(); cur.ep(acc, wr, wc, l2 & 15, l2 >> 4); }
;         if (!has_next) break;
;         cur = nxt;
.LBB0_873:
	s_xor_b64 s[24:25], s[16:17], -1
	s_andn2_b64 vcc, exec, s[16:17]
	s_mov_b32 s97, s42
	s_mov_b32 s45, s6
	s_mov_b32 s69, s96
	s_mov_b64 s[64:65], s[58:59]
	s_mov_b64 s[38:39], s[60:61]
	s_mov_b64 s[26:27], s[62:63]
	s_mov_b64 s[66:67], s[30:31]
	s_cbranch_vccnz .LBB0_875
	s_add_i32 s16, s19, s43
	s_ashr_i32 s17, s16, 31
	s_lshl_b64 s[16:17], s[16:17], 12
	s_add_u32 s52, s50, s16
	s_addc_u32 s53, s51, s17
	s_ashr_i32 s9, s8, 31
	s_lshl_b64 s[16:17], s[8:9], 24
	s_add_u32 s9, s12, s16
	s_addc_u32 s26, s13, s17
	s_ashr_i32 s19, s18, 31
	s_lshl_b64 s[16:17], s[18:19], 2
	s_add_u32 s54, s9, s16
	s_addc_u32 s55, s26, s17
	s_add_u32 s56, s54, 0x200
	s_addc_u32 s57, s55, 0
	s_lshl_b32 s16, s8, 11
	s_ashr_i32 s17, s16, 31
	s_lshl_b64 s[16:17], s[16:17], 2
	s_add_u32 s26, s14, s16
	s_addc_u32 s27, s15, s17
	s_lshl_b32 s8, s8, 13
	s_ashr_i32 s9, s8, 31
	s_lshl_b64 s[8:9], s[8:9], 2
	s_add_u32 s38, s74, s8
	s_addc_u32 s39, s75, s9
	s_add_u32 s64, s4, s8
	s_addc_u32 s65, s5, s9
	s_mov_b32 s97, s18
	s_mov_b32 s45, s36
	s_mov_b32 s69, s43
	s_mul_i32 s100, s72, 0x90
	s_sub_i32 s99, s36, s43
	s_sub_i32 s99, s99, s100
	s_add_i32 s99, s99, 15
	s_max_i32 s99, s99, 0
	s_lshr_b32 s99, s99, 4
	s_min_u32 s99, s99, 9
	s_mov_b64 s[66:67], s[40:41]

; __global__ void __launch_bounds__(NTHR, 2) hybrid_fwd(Params P) {
	.amdhsa_kernel _ZN12_GLOBAL__N_110hybrid_fwdENS_6ParamsE
		.amdhsa_group_segment_fixed_size 0
		.amdhsa_private_segment_fixed_size 0
		.amdhsa_kernarg_size 488
		.amdhsa_user_sgpr_count 2
		.amdhsa_user_sgpr_dispatch_ptr 0
		.amdhsa_user_sgpr_queue_ptr 0
		.amdhsa_user_sgpr_kernarg_segment_ptr 1
		.amdhsa_user_sgpr_dispatch_id 0
		.amdhsa_user_sgpr_kernarg_preload_length 0
		.amdhsa_user_sgpr_kernarg_preload_offset 0
		.amdhsa_user_sgpr_private_segment_size 0
		.amdhsa_uses_dynamic_stack 0
		.amdhsa_enable_private_segment 0
		.amdhsa_system_sgpr_workgroup_id_x 1
		.amdhsa_system_sgpr_workgroup_id_y 0
		.amdhsa_system_sgpr_workgroup_id_z 0
		.amdhsa_system_sgpr_workgroup_info 0
		.amdhsa_system_vgpr_workitem_id 0
		.amdhsa_next_free_vgpr 256
		.amdhsa_next_free_sgpr 102
		.amdhsa_accum_offset 256
		.amdhsa_reserve_vcc 1
		.amdhsa_float_round_mode_32 0
		.amdhsa_float_round_mode_16_64 0
		.amdhsa_float_denorm_mode_32 3
		.amdhsa_float_denorm_mode_16_64 3
		.amdhsa_dx10_clamp 1
		.amdhsa_ieee_mode 1
		.amdhsa_fp16_overflow 0
		.amdhsa_tg_split 0
		.amdhsa_exception_fp_ieee_invalid_op 0
		.amdhsa_exception_fp_denorm_src 0
		.amdhsa_exception_fp_ieee_div_zero 0
		.amdhsa_exception_fp_ieee_overflow 0
		.amdhsa_exception_fp_ieee_underflow 0
		.amdhsa_exception_fp_ieee_inexact 0
		.amdhsa_exception_int_div_zero 0
	.end_amdhsa_kernel

; __global__ void __launch_bounds__(NTHR, 2) hybrid_fwd(Params P) {
amdhsa.kernels:
  - .agpr_count:     0
    .args:
      - .offset:         0
        .size:           232
        .value_kind:     by_value
      - .offset:         232
        .size:           4
        .value_kind:     hidden_block_count_x
      - .offset:         236
        .size:           4
        .value_kind:     hidden_block_count_y
      - .offset:         240
        .size:           4
        .value_kind:     hidden_block_count_z
      - .offset:         244
        .size:           2
        .value_kind:     hidden_group_size_x
      - .offset:         246
        .size:           2
        .value_kind:     hidden_group_size_y
      - .offset:         248
        .size:           2
        .value_kind:     hidden_group_size_z
      - .offset:         250
        .size:           2
        .value_kind:     hidden_remainder_x
      - .offset:         252
        .size:           2
        .value_kind:     hidden_remainder_y
      - .offset:         254
        .size:           2
        .value_kind:     hidden_remainder_z
      - .offset:         272
        .size:           8
        .value_kind:     hidden_global_offset_x
      - .offset:         280
        .size:           8
        .value_kind:     hidden_global_offset_y
      - .offset:         288
        .size:           8
        .value_kind:     hidden_global_offset_z
      - .offset:         296
        .size:           2
        .value_kind:     hidden_grid_dims
      - .offset:         352
        .size:           4
        .value_kind:     hidden_dynamic_lds_size
    .group_segment_fixed_size: 0
    .kernarg_segment_align: 8
    .kernarg_segment_size: 488
    .language:       OpenCL C
    .language_version:
      - 2
      - 0
    .max_flat_workgroup_size: 512
    .name:           _ZN12_GLOBAL__N_110hybrid_fwdENS_6ParamsE
    .private_segment_fixed_size: 0
    .sgpr_count:     108
    .sgpr_spill_count: 18
    .symbol:         _ZN12_GLOBAL__N_110hybrid_fwdENS_6ParamsE.kd
    .uniform_work_group_size: 1
    .uses_dynamic_stack: false
    .vgpr_count:     256
    .vgpr_spill_count: 0
    .wavefront_size: 64
